# agg1 rewritten by hand: row-per-node layout (4 nodes per wave), pad-row masking, no phi copies, first-stage specialisation
# speedup vs baseline: 1.1393x; 1.1393x over previous
_Z13second_kernelPKfPKDF16_PDF16_PfS4_PKjPKiPiS9_:
	s_cmp_lg_u32 s2, 0
	s_cbranch_scc1 .Lsk_nopad
	s_load_dwordx4 s[4:7], s[0:1], 0x10
	v_lshlrev_b32_e32 v1, 2, v0
	v_mov_b32_e32 v2, 0
	v_mov_b32_e32 v3, 0xfc00fc00
	s_waitcnt lgkmcnt(0)
	s_add_u32 s4, s4, 0x61a800
	s_addc_u32 s5, s5, 0
	s_add_u32 s6, s6, 0xc3500
	s_addc_u32 s7, s7, 0
	v_cmp_gt_u32_e32 vcc, 32, v0
	s_and_saveexec_b64 s[8:9], vcc
	global_store_dword v1, v2, s[4:5]
	v_cmp_gt_u32_e32 vcc, 4, v0
	s_and_b64 exec, exec, vcc
	global_store_dword v1, v3, s[6:7]
	s_mov_b64 exec, s[8:9]
.Lsk_nopad:
	s_cmpk_gt_u32 s2, 0x186
	s_mov_b64 s[4:5], -1
	s_cbranch_scc0 .LBB1_69
	s_movk_i32 s3, 0x80
	v_cmp_gt_u32_e64 s[12:13], s3, v0
	v_lshlrev_b32_e32 v1, 2, v0
	s_and_saveexec_b64 s[4:5], s[12:13]
	v_mov_b32_e32 v2, 0
	ds_write_b32 v1, v2 offset:3600
	s_or_b64 exec, exec, s[4:5]
	s_movk_i32 s4, 0x7d
	s_add_i32 s3, s2, 0xfffffe79
	v_cmp_gt_u32_e32 vcc, s4, v0
	v_mov_b32_e32 v2, 0
	v_mov_b32_e32 v3, 0
	v_mov_b32_e32 v4, 0
	s_and_saveexec_b64 s[4:5], vcc
	s_cbranch_execz .LBB1_5
	s_load_dwordx2 s[6:7], s[0:1], 0x30
	s_lshl_b32 s8, s3, 7
	v_or_b32_e32 v4, s8, v0
	s_addk_i32 s8, 0x80
	v_ashrrev_i32_e32 v5, 31, v4
	v_or_b32_e32 v6, s8, v0
	s_waitcnt lgkmcnt(0)
	v_lshl_add_u64 v[4:5], v[4:5], 2, s[6:7]
	v_ashrrev_i32_e32 v7, 31, v6
	v_lshl_add_u64 v[6:7], v[6:7], 2, s[6:7]
	global_load_dword v3, v[4:5], off
	global_load_dword v8, v[6:7], off
	s_movk_i32 s6, 0x1900
	s_waitcnt vmcnt(1)
	v_mad_u32_u24 v5, v0, s6, v3
	s_waitcnt vmcnt(0)
	v_sub_u32_e32 v4, v8, v3
	ds_write_b32 v1, v5 offset:2048

_Z11agg1_kernelPKDF16_PKfS2_PKiS4_S2_S2_PDF16_PfS6_i:
	s_load_dwordx8 s[4:11], s[0:1], 0x0
	s_load_dwordx8 s[12:19], s[0:1], 0x20
	s_load_dwordx4 s[20:23], s[0:1], 0x40
	s_load_dword s24, s[0:1], 0x50
	v_lshlrev_b32_e32 v22, 2, v0
	v_readfirstlane_b32 s25, v0
	s_lshl_b32 s26, s2, 5
	s_waitcnt lgkmcnt(0)
	global_load_dword v23, v22, s[14:15]
	global_load_dword v24, v22, s[16:17]
	s_lshr_b32 s25, s25, 6
	s_lshl_b32 s27, s25, 3
	s_add_i32 s26, s26, s27
	s_cmp_le_i32 s24, s26
	s_waitcnt vmcnt(0)
	ds_write2st64_b32 v22, v23, v24 offset0:32 offset1:36
	s_waitcnt lgkmcnt(0)
	s_barrier
	s_cbranch_scc1 .Lagg_exit
	v_and_b32_e32 v53, 15, v0
	v_bfe_u32 v4, v0, 4, 2
	v_and_b32_e32 v1, 14, v0
	v_and_b32_e32 v2, 1, v0
	v_lshlrev_b32_e32 v2, 3, v2
	v_lshlrev_b32_e32 v54, 1, v1
	v_lshlrev_b32_e32 v3, 7, v53
	v_lshl_add_u32 v3, v4, 1, v3
	s_lshl_b32 s27, s25, 11
	v_add_u32_e32 v3, s27, v3
	v_lshlrev_b32_e32 v52, 5, v53
	v_add_u32_e32 v52, 0x2000, v52
	v_cmp_eq_u32_e64 s[34:35], 0, v53
	v_and_b32_e32 v5, 63, v0
	v_lshlrev_b32_e32 v5, 5, v5
	v_add_u32_e32 v55, s27, v5
	v_mov_b32_e32 v8, 0
	v_mov_b32_e32 v9, 0
	v_mov_b32_e32 v10, 0
	v_mov_b32_e32 v11, 0
	ds_write_b128 v55, v[8:11]
	ds_write_b128 v55, v[8:11] offset:16
	s_add_i32 s28, s24, -1
	v_add_u32_e32 v22, s26, v4
	v_add_u32_e32 v23, 4, v22
	v_cmp_gt_i32_e64 s[36:37], s24, v22
	v_cmp_gt_i32_e64 s[38:39], s24, v23
	v_min_i32_e32 v22, s28, v22
	v_min_i32_e32 v23, s28, v23
	v_lshlrev_b32_e32 v24, 2, v22
	v_lshlrev_b32_e32 v25, 2, v23
	global_load_dword v48, v24, s[10:11]
	global_load_dword v26, v24, s[10:11] offset:4
	global_load_dword v50, v25, s[10:11]
	global_load_dword v27, v25, s[10:11] offset:4
	v_lshl_or_b32 v28, v22, 5, v54
	v_lshl_or_b32 v29, v23, 5, v54
	global_load_dword v7, v28, s[8:9]
	global_load_dword v10, v29, s[8:9]
	v_mov_b32_e32 v4, v24
	s_waitcnt vmcnt(2)
	v_sub_u32_e32 v49, v26, v48
	v_sub_u32_e32 v51, v27, v50
	v_add_u32_e32 v49, 1, v49
	v_add_u32_e32 v51, 1, v51
	s_nop 0
	v_readlane_b32 s29, v49, 0
	v_readlane_b32 s27, v49, 16
	v_readlane_b32 s40, v49, 32
	v_readlane_b32 s41, v49, 48
	s_max_i32 s29, s29, s27
	s_max_i32 s40, s40, s41
	s_max_i32 s29, s29, s40
	v_readlane_b32 s30, v51, 0
	v_readlane_b32 s27, v51, 16
	v_readlane_b32 s40, v51, 32
	v_readlane_b32 s41, v51, 48
	s_max_i32 s30, s30, s27
	s_max_i32 s40, s40, s41
	s_max_i32 s30, s30, s40
	v_add_u32_e32 v30, v48, v53
	v_lshlrev_b32_e32 v30, 2, v30
	v_mov_b32_e32 v5, s24
	v_mov_b32_e32 v6, s24
	v_cndmask_b32_e64 v5, v5, v22, s[34:35]
	v_cmp_gt_i32_e32 vcc, v49, v53
	s_andn2_b64 s[40:41], vcc, s[34:35]
	s_and_saveexec_b64 s[32:33], s[40:41]
	global_load_dword v5, v30, s[12:13] offset:-4
	s_mov_b64 exec, s[32:33]
	v_add_u32_e32 v31, 16, v53
	v_cmp_gt_i32_e32 vcc, v49, v31
	s_and_saveexec_b64 s[32:33], vcc
	global_load_dword v6, v30, s[12:13] offset:60
	s_mov_b64 exec, s[32:33]
	v_add_u32_e32 v30, v50, v53
	v_lshlrev_b32_e32 v30, 2, v30
	v_mov_b32_e32 v8, s24
	v_mov_b32_e32 v9, s24
	v_cndmask_b32_e64 v8, v8, v23, s[34:35]
	v_cmp_gt_i32_e32 vcc, v51, v53
	s_andn2_b64 s[40:41], vcc, s[34:35]
	s_and_saveexec_b64 s[32:33], s[40:41]
	global_load_dword v8, v30, s[12:13] offset:-4
	s_mov_b64 exec, s[32:33]
	v_add_u32_e32 v31, 16, v53
	v_cmp_gt_i32_e32 vcc, v51, v31
	s_and_saveexec_b64 s[32:33], vcc
	global_load_dword v9, v30, s[12:13] offset:60
	s_mov_b64 exec, s[32:33]
	s_waitcnt vmcnt(0)
	v_lshlrev_b32_e32 v5, 4, v5
	v_lshlrev_b32_e32 v6, 4, v6
	v_lshlrev_b32_e32 v8, 4, v8
	v_lshlrev_b32_e32 v9, 4, v9
	s_mov_b32 s31, 0
.Lagg_batch:
	s_mov_b32 s42, 0
	s_cmp_lt_i32 s29, 3
	s_cbranch_scc1 .Lagg_s0h
	v_or_b32_dpp v22, v5, v1 row_newbcast:0 row_mask:0xf bank_mask:0xf
	v_or_b32_dpp v23, v5, v1 row_newbcast:1 row_mask:0xf bank_mask:0xf
	v_or_b32_dpp v24, v5, v1 row_newbcast:2 row_mask:0xf bank_mask:0xf
	v_or_b32_dpp v25, v5, v1 row_newbcast:3 row_mask:0xf bank_mask:0xf
	global_load_ushort v30, v22, s[6:7]
	global_load_ushort v31, v23, s[6:7]
	global_load_ushort v32, v24, s[6:7]
	global_load_ushort v33, v25, s[6:7]
	v_lshl_or_b32 v26, v22, 3, v2
	v_lshl_or_b32 v27, v23, 3, v2
	v_lshl_or_b32 v28, v24, 3, v2
	v_lshl_or_b32 v29, v25, 3, v2
	global_load_dwordx2 v[34:35], v26, s[4:5]
	global_load_dwordx2 v[36:37], v27, s[4:5]
	global_load_dwordx2 v[38:39], v28, s[4:5]
	global_load_dwordx2 v[40:41], v29, s[4:5]
	s_waitcnt vmcnt(4)
	v_fma_mix_f32 v30, v30, 1.0, v7 op_sel_hi:[1,0,0]
	v_fma_mix_f32 v31, v31, 1.0, v7 op_sel_hi:[1,0,0]
	v_fma_mix_f32 v32, v32, 1.0, v7 op_sel_hi:[1,0,0]
	v_fma_mix_f32 v33, v33, 1.0, v7 op_sel_hi:[1,0,0]
	v_mul_f32_e32 v44, 0x3e4ccccd, v30
	v_mul_f32_e32 v45, 0x3e4ccccd, v31
	v_mul_f32_e32 v46, 0x3e4ccccd, v32
	v_mul_f32_e32 v47, 0x3e4ccccd, v33
	v_max_f32_e32 v30, v30, v44
	v_max_f32_e32 v31, v31, v45
	v_max_f32_e32 v32, v32, v46
	v_max_f32_e32 v33, v33, v47
	v_max3_f32 v42, v30, v31, v32
	v_max_f32_e32 v12, v42, v33
	v_sub_f32_e32 v30, v30, v12
	v_sub_f32_e32 v31, v31, v12
	v_sub_f32_e32 v32, v32, v12
	v_sub_f32_e32 v33, v33, v12
	v_exp_f32_e32 v30, v30
	v_exp_f32_e32 v31, v31
	v_exp_f32_e32 v32, v32
	v_exp_f32_e32 v33, v33
	s_nop 0
	v_add_f32_e32 v13, v30, v31
	v_add_f32_e32 v13, v13, v32
	v_add_f32_e32 v13, v13, v33
	s_waitcnt vmcnt(3)
	v_cvt_scalef32_pk_f16_fp8 v44, v34, 1.0
	v_cvt_scalef32_pk_f16_fp8 v45, v34, 1.0 op_sel:[1,0,0]
	v_cvt_scalef32_pk_f16_fp8 v46, v35, 1.0
	v_cvt_scalef32_pk_f16_fp8 v47, v35, 1.0 op_sel:[1,0,0]
	v_fma_mix_f32 v14, v44, v30, 0 op_sel_hi:[1,0,0]
	v_fma_mix_f32 v15, v44, v30, 0 op_sel:[1,0,0] op_sel_hi:[1,0,0]
	v_fma_mix_f32 v16, v45, v30, 0 op_sel_hi:[1,0,0]
	v_fma_mix_f32 v17, v45, v30, 0 op_sel:[1,0,0] op_sel_hi:[1,0,0]
	v_fma_mix_f32 v18, v46, v30, 0 op_sel_hi:[1,0,0]
	v_fma_mix_f32 v19, v46, v30, 0 op_sel:[1,0,0] op_sel_hi:[1,0,0]
	v_fma_mix_f32 v20, v47, v30, 0 op_sel_hi:[1,0,0]
	v_fma_mix_f32 v21, v47, v30, 0 op_sel:[1,0,0] op_sel_hi:[1,0,0]
	s_waitcnt vmcnt(2)
	v_cvt_scalef32_pk_f16_fp8 v44, v36, 1.0
	v_cvt_scalef32_pk_f16_fp8 v45, v36, 1.0 op_sel:[1,0,0]
	v_cvt_scalef32_pk_f16_fp8 v46, v37, 1.0
	v_cvt_scalef32_pk_f16_fp8 v47, v37, 1.0 op_sel:[1,0,0]
	v_fma_mix_f32 v14, v44, v31, v14 op_sel_hi:[1,0,0]
	v_fma_mix_f32 v15, v44, v31, v15 op_sel:[1,0,0] op_sel_hi:[1,0,0]
	v_fma_mix_f32 v16, v45, v31, v16 op_sel_hi:[1,0,0]
	v_fma_mix_f32 v17, v45, v31, v17 op_sel:[1,0,0] op_sel_hi:[1,0,0]
	v_fma_mix_f32 v18, v46, v31, v18 op_sel_hi:[1,0,0]
	v_fma_mix_f32 v19, v46, v31, v19 op_sel:[1,0,0] op_sel_hi:[1,0,0]
	v_fma_mix_f32 v20, v47, v31, v20 op_sel_hi:[1,0,0]
	v_fma_mix_f32 v21, v47, v31, v21 op_sel:[1,0,0] op_sel_hi:[1,0,0]
	s_waitcnt vmcnt(1)
	v_cvt_scalef32_pk_f16_fp8 v44, v38, 1.0
	v_cvt_scalef32_pk_f16_fp8 v45, v38, 1.0 op_sel:[1,0,0]
	v_cvt_scalef32_pk_f16_fp8 v46, v39, 1.0
	v_cvt_scalef32_pk_f16_fp8 v47, v39, 1.0 op_sel:[1,0,0]
	v_fma_mix_f32 v14, v44, v32, v14 op_sel_hi:[1,0,0]
	v_fma_mix_f32 v15, v44, v32, v15 op_sel:[1,0,0] op_sel_hi:[1,0,0]
	v_fma_mix_f32 v16, v45, v32, v16 op_sel_hi:[1,0,0]
	v_fma_mix_f32 v17, v45, v32, v17 op_sel:[1,0,0] op_sel_hi:[1,0,0]
	v_fma_mix_f32 v18, v46, v32, v18 op_sel_hi:[1,0,0]
	v_fma_mix_f32 v19, v46, v32, v19 op_sel:[1,0,0] op_sel_hi:[1,0,0]
	v_fma_mix_f32 v20, v47, v32, v20 op_sel_hi:[1,0,0]
	v_fma_mix_f32 v21, v47, v32, v21 op_sel:[1,0,0] op_sel_hi:[1,0,0]
	s_waitcnt vmcnt(0)
	v_cvt_scalef32_pk_f16_fp8 v44, v40, 1.0
	v_cvt_scalef32_pk_f16_fp8 v45, v40, 1.0 op_sel:[1,0,0]
	v_cvt_scalef32_pk_f16_fp8 v46, v41, 1.0
	v_cvt_scalef32_pk_f16_fp8 v47, v41, 1.0 op_sel:[1,0,0]
	v_fma_mix_f32 v14, v44, v33, v14 op_sel_hi:[1,0,0]
	v_fma_mix_f32 v15, v44, v33, v15 op_sel:[1,0,0] op_sel_hi:[1,0,0]
	v_fma_mix_f32 v16, v45, v33, v16 op_sel_hi:[1,0,0]
	v_fma_mix_f32 v17, v45, v33, v17 op_sel:[1,0,0] op_sel_hi:[1,0,0]
	v_fma_mix_f32 v18, v46, v33, v18 op_sel_hi:[1,0,0]
	v_fma_mix_f32 v19, v46, v33, v19 op_sel:[1,0,0] op_sel_hi:[1,0,0]
	v_fma_mix_f32 v20, v47, v33, v20 op_sel_hi:[1,0,0]
	v_fma_mix_f32 v21, v47, v33, v21 op_sel:[1,0,0] op_sel_hi:[1,0,0]
	s_branch .Lagg_c1
.Lagg_s0h:
	v_or_b32_dpp v22, v5, v1 row_newbcast:0 row_mask:0xf bank_mask:0xf
	v_or_b32_dpp v23, v5, v1 row_newbcast:1 row_mask:0xf bank_mask:0xf
	global_load_ushort v30, v22, s[6:7]
	global_load_ushort v31, v23, s[6:7]
	v_lshl_or_b32 v26, v22, 3, v2
	v_lshl_or_b32 v27, v23, 3, v2
	global_load_dwordx2 v[34:35], v26, s[4:5]
	global_load_dwordx2 v[36:37], v27, s[4:5]
	s_waitcnt vmcnt(2)
	v_fma_mix_f32 v30, v30, 1.0, v7 op_sel_hi:[1,0,0]
	v_fma_mix_f32 v31, v31, 1.0, v7 op_sel_hi:[1,0,0]
	v_mul_f32_e32 v44, 0x3e4ccccd, v30
	v_mul_f32_e32 v45, 0x3e4ccccd, v31
	v_max_f32_e32 v30, v30, v44
	v_max_f32_e32 v31, v31, v45
	v_max_f32_e32 v12, v30, v31
	v_sub_f32_e32 v30, v30, v12
	v_sub_f32_e32 v31, v31, v12
	v_exp_f32_e32 v30, v30
	v_exp_f32_e32 v31, v31
	s_nop 0
	v_add_f32_e32 v13, v30, v31
	s_waitcnt vmcnt(1)
	v_cvt_scalef32_pk_f16_fp8 v44, v34, 1.0
	v_cvt_scalef32_pk_f16_fp8 v45, v34, 1.0 op_sel:[1,0,0]
	v_cvt_scalef32_pk_f16_fp8 v46, v35, 1.0
	v_cvt_scalef32_pk_f16_fp8 v47, v35, 1.0 op_sel:[1,0,0]
	v_fma_mix_f32 v14, v44, v30, 0 op_sel_hi:[1,0,0]
	v_fma_mix_f32 v15, v44, v30, 0 op_sel:[1,0,0] op_sel_hi:[1,0,0]
	v_fma_mix_f32 v16, v45, v30, 0 op_sel_hi:[1,0,0]
	v_fma_mix_f32 v17, v45, v30, 0 op_sel:[1,0,0] op_sel_hi:[1,0,0]
	v_fma_mix_f32 v18, v46, v30, 0 op_sel_hi:[1,0,0]
	v_fma_mix_f32 v19, v46, v30, 0 op_sel:[1,0,0] op_sel_hi:[1,0,0]
	v_fma_mix_f32 v20, v47, v30, 0 op_sel_hi:[1,0,0]
	v_fma_mix_f32 v21, v47, v30, 0 op_sel:[1,0,0] op_sel_hi:[1,0,0]
	s_waitcnt vmcnt(0)
	v_cvt_scalef32_pk_f16_fp8 v44, v36, 1.0
	v_cvt_scalef32_pk_f16_fp8 v45, v36, 1.0 op_sel:[1,0,0]
	v_cvt_scalef32_pk_f16_fp8 v46, v37, 1.0
	v_cvt_scalef32_pk_f16_fp8 v47, v37, 1.0 op_sel:[1,0,0]
	v_fma_mix_f32 v14, v44, v31, v14 op_sel_hi:[1,0,0]
	v_fma_mix_f32 v15, v44, v31, v15 op_sel:[1,0,0] op_sel_hi:[1,0,0]
	v_fma_mix_f32 v16, v45, v31, v16 op_sel_hi:[1,0,0]
	v_fma_mix_f32 v17, v45, v31, v17 op_sel:[1,0,0] op_sel_hi:[1,0,0]
	v_fma_mix_f32 v18, v46, v31, v18 op_sel_hi:[1,0,0]
	v_fma_mix_f32 v19, v46, v31, v19 op_sel:[1,0,0] op_sel_hi:[1,0,0]
	v_fma_mix_f32 v20, v47, v31, v20 op_sel_hi:[1,0,0]
	v_fma_mix_f32 v21, v47, v31, v21 op_sel:[1,0,0] op_sel_hi:[1,0,0]
	s_branch .Lagg_epi
.Lagg_c1:
	s_cmp_lt_i32 s29, 5
	s_cbranch_scc1 .Lagg_epi
	s_cmp_lt_i32 s29, 7
	s_cbranch_scc1 .Lagg_s1h
	v_or_b32_dpp v22, v5, v1 row_newbcast:4 row_mask:0xf bank_mask:0xf
	v_or_b32_dpp v23, v5, v1 row_newbcast:5 row_mask:0xf bank_mask:0xf
	v_or_b32_dpp v24, v5, v1 row_newbcast:6 row_mask:0xf bank_mask:0xf
	v_or_b32_dpp v25, v5, v1 row_newbcast:7 row_mask:0xf bank_mask:0xf
	global_load_ushort v30, v22, s[6:7]
	global_load_ushort v31, v23, s[6:7]
	global_load_ushort v32, v24, s[6:7]
	global_load_ushort v33, v25, s[6:7]
	v_lshl_or_b32 v26, v22, 3, v2
	v_lshl_or_b32 v27, v23, 3, v2
	v_lshl_or_b32 v28, v24, 3, v2
	v_lshl_or_b32 v29, v25, 3, v2
	global_load_dwordx2 v[34:35], v26, s[4:5]
	global_load_dwordx2 v[36:37], v27, s[4:5]
	global_load_dwordx2 v[38:39], v28, s[4:5]
	global_load_dwordx2 v[40:41], v29, s[4:5]
	s_waitcnt vmcnt(4)
	v_fma_mix_f32 v30, v30, 1.0, v7 op_sel_hi:[1,0,0]
	v_fma_mix_f32 v31, v31, 1.0, v7 op_sel_hi:[1,0,0]
	v_fma_mix_f32 v32, v32, 1.0, v7 op_sel_hi:[1,0,0]
	v_fma_mix_f32 v33, v33, 1.0, v7 op_sel_hi:[1,0,0]
	v_mul_f32_e32 v44, 0x3e4ccccd, v30
	v_mul_f32_e32 v45, 0x3e4ccccd, v31
	v_mul_f32_e32 v46, 0x3e4ccccd, v32
	v_mul_f32_e32 v47, 0x3e4ccccd, v33
	v_max_f32_e32 v30, v30, v44
	v_max_f32_e32 v31, v31, v45
	v_max_f32_e32 v32, v32, v46
	v_max_f32_e32 v33, v33, v47
	v_max3_f32 v42, v12, v30, v31
	v_max3_f32 v11, v42, v32, v33
	v_sub_f32_e32 v43, v12, v11
	v_sub_f32_e32 v30, v30, v11
	v_sub_f32_e32 v31, v31, v11
	v_sub_f32_e32 v32, v32, v11
	v_sub_f32_e32 v33, v33, v11
	v_exp_f32_e32 v43, v43
	v_exp_f32_e32 v30, v30
	v_exp_f32_e32 v31, v31
	v_exp_f32_e32 v32, v32
	v_exp_f32_e32 v33, v33
	v_fma_f32 v13, v13, v43, v30
	v_mul_f32_e32 v14, v14, v43
	v_mul_f32_e32 v15, v15, v43
	v_mul_f32_e32 v16, v16, v43
	v_mul_f32_e32 v17, v17, v43
	v_mul_f32_e32 v18, v18, v43
	v_mul_f32_e32 v19, v19, v43
	v_mul_f32_e32 v20, v20, v43
	v_mul_f32_e32 v21, v21, v43
	v_add_f32_e32 v13, v13, v31
	v_add_f32_e32 v13, v13, v32
	v_add_f32_e32 v13, v13, v33
	s_waitcnt vmcnt(3)
	v_cvt_scalef32_pk_f16_fp8 v44, v34, 1.0
	v_cvt_scalef32_pk_f16_fp8 v45, v34, 1.0 op_sel:[1,0,0]
	v_cvt_scalef32_pk_f16_fp8 v46, v35, 1.0
	v_cvt_scalef32_pk_f16_fp8 v47, v35, 1.0 op_sel:[1,0,0]
	v_fma_mix_f32 v14, v44, v30, v14 op_sel_hi:[1,0,0]
	v_fma_mix_f32 v15, v44, v30, v15 op_sel:[1,0,0] op_sel_hi:[1,0,0]
	v_fma_mix_f32 v16, v45, v30, v16 op_sel_hi:[1,0,0]
	v_fma_mix_f32 v17, v45, v30, v17 op_sel:[1,0,0] op_sel_hi:[1,0,0]
	v_fma_mix_f32 v18, v46, v30, v18 op_sel_hi:[1,0,0]
	v_fma_mix_f32 v19, v46, v30, v19 op_sel:[1,0,0] op_sel_hi:[1,0,0]
	v_fma_mix_f32 v20, v47, v30, v20 op_sel_hi:[1,0,0]
	v_fma_mix_f32 v21, v47, v30, v21 op_sel:[1,0,0] op_sel_hi:[1,0,0]
	s_waitcnt vmcnt(2)
	v_cvt_scalef32_pk_f16_fp8 v44, v36, 1.0
	v_cvt_scalef32_pk_f16_fp8 v45, v36, 1.0 op_sel:[1,0,0]
	v_cvt_scalef32_pk_f16_fp8 v46, v37, 1.0
	v_cvt_scalef32_pk_f16_fp8 v47, v37, 1.0 op_sel:[1,0,0]
	v_fma_mix_f32 v14, v44, v31, v14 op_sel_hi:[1,0,0]
	v_fma_mix_f32 v15, v44, v31, v15 op_sel:[1,0,0] op_sel_hi:[1,0,0]
	v_fma_mix_f32 v16, v45, v31, v16 op_sel_hi:[1,0,0]
	v_fma_mix_f32 v17, v45, v31, v17 op_sel:[1,0,0] op_sel_hi:[1,0,0]
	v_fma_mix_f32 v18, v46, v31, v18 op_sel_hi:[1,0,0]
	v_fma_mix_f32 v19, v46, v31, v19 op_sel:[1,0,0] op_sel_hi:[1,0,0]
	v_fma_mix_f32 v20, v47, v31, v20 op_sel_hi:[1,0,0]
	v_fma_mix_f32 v21, v47, v31, v21 op_sel:[1,0,0] op_sel_hi:[1,0,0]
	s_waitcnt vmcnt(1)
	v_cvt_scalef32_pk_f16_fp8 v44, v38, 1.0
	v_cvt_scalef32_pk_f16_fp8 v45, v38, 1.0 op_sel:[1,0,0]
	v_cvt_scalef32_pk_f16_fp8 v46, v39, 1.0
	v_cvt_scalef32_pk_f16_fp8 v47, v39, 1.0 op_sel:[1,0,0]
	v_fma_mix_f32 v14, v44, v32, v14 op_sel_hi:[1,0,0]
	v_fma_mix_f32 v15, v44, v32, v15 op_sel:[1,0,0] op_sel_hi:[1,0,0]
	v_fma_mix_f32 v16, v45, v32, v16 op_sel_hi:[1,0,0]
	v_fma_mix_f32 v17, v45, v32, v17 op_sel:[1,0,0] op_sel_hi:[1,0,0]
	v_fma_mix_f32 v18, v46, v32, v18 op_sel_hi:[1,0,0]
	v_fma_mix_f32 v19, v46, v32, v19 op_sel:[1,0,0] op_sel_hi:[1,0,0]
	v_fma_mix_f32 v20, v47, v32, v20 op_sel_hi:[1,0,0]
	v_fma_mix_f32 v21, v47, v32, v21 op_sel:[1,0,0] op_sel_hi:[1,0,0]
	s_waitcnt vmcnt(0)
	v_cvt_scalef32_pk_f16_fp8 v44, v40, 1.0
	v_cvt_scalef32_pk_f16_fp8 v45, v40, 1.0 op_sel:[1,0,0]
	v_cvt_scalef32_pk_f16_fp8 v46, v41, 1.0
	v_cvt_scalef32_pk_f16_fp8 v47, v41, 1.0 op_sel:[1,0,0]
	v_fma_mix_f32 v14, v44, v33, v14 op_sel_hi:[1,0,0]
	v_fma_mix_f32 v15, v44, v33, v15 op_sel:[1,0,0] op_sel_hi:[1,0,0]
	v_fma_mix_f32 v16, v45, v33, v16 op_sel_hi:[1,0,0]
	v_fma_mix_f32 v17, v45, v33, v17 op_sel:[1,0,0] op_sel_hi:[1,0,0]
	v_fma_mix_f32 v18, v46, v33, v18 op_sel_hi:[1,0,0]
	v_fma_mix_f32 v19, v46, v33, v19 op_sel:[1,0,0] op_sel_hi:[1,0,0]
	v_fma_mix_f32 v20, v47, v33, v20 op_sel_hi:[1,0,0]
	v_fma_mix_f32 v21, v47, v33, v21 op_sel:[1,0,0] op_sel_hi:[1,0,0]
	s_branch .Lagg_d1
.Lagg_s1h:
	v_or_b32_dpp v22, v5, v1 row_newbcast:4 row_mask:0xf bank_mask:0xf
	v_or_b32_dpp v23, v5, v1 row_newbcast:5 row_mask:0xf bank_mask:0xf
	global_load_ushort v30, v22, s[6:7]
	global_load_ushort v31, v23, s[6:7]
	v_lshl_or_b32 v26, v22, 3, v2
	v_lshl_or_b32 v27, v23, 3, v2
	global_load_dwordx2 v[34:35], v26, s[4:5]
	global_load_dwordx2 v[36:37], v27, s[4:5]
	s_waitcnt vmcnt(2)
	v_fma_mix_f32 v30, v30, 1.0, v7 op_sel_hi:[1,0,0]
	v_fma_mix_f32 v31, v31, 1.0, v7 op_sel_hi:[1,0,0]
	v_mul_f32_e32 v44, 0x3e4ccccd, v30
	v_mul_f32_e32 v45, 0x3e4ccccd, v31
	v_max_f32_e32 v30, v30, v44
	v_max_f32_e32 v31, v31, v45
	v_max3_f32 v11, v12, v30, v31
	v_sub_f32_e32 v43, v12, v11
	v_sub_f32_e32 v30, v30, v11
	v_sub_f32_e32 v31, v31, v11
	v_exp_f32_e32 v43, v43
	v_exp_f32_e32 v30, v30
	v_exp_f32_e32 v31, v31
	v_fma_f32 v13, v13, v43, v30
	v_mul_f32_e32 v14, v14, v43
	v_mul_f32_e32 v15, v15, v43
	v_mul_f32_e32 v16, v16, v43
	v_mul_f32_e32 v17, v17, v43
	v_mul_f32_e32 v18, v18, v43
	v_mul_f32_e32 v19, v19, v43
	v_mul_f32_e32 v20, v20, v43
	v_mul_f32_e32 v21, v21, v43
	v_add_f32_e32 v13, v13, v31
	s_waitcnt vmcnt(1)
	v_cvt_scalef32_pk_f16_fp8 v44, v34, 1.0
	v_cvt_scalef32_pk_f16_fp8 v45, v34, 1.0 op_sel:[1,0,0]
	v_cvt_scalef32_pk_f16_fp8 v46, v35, 1.0
	v_cvt_scalef32_pk_f16_fp8 v47, v35, 1.0 op_sel:[1,0,0]
	v_fma_mix_f32 v14, v44, v30, v14 op_sel_hi:[1,0,0]
	v_fma_mix_f32 v15, v44, v30, v15 op_sel:[1,0,0] op_sel_hi:[1,0,0]
	v_fma_mix_f32 v16, v45, v30, v16 op_sel_hi:[1,0,0]
	v_fma_mix_f32 v17, v45, v30, v17 op_sel:[1,0,0] op_sel_hi:[1,0,0]
	v_fma_mix_f32 v18, v46, v30, v18 op_sel_hi:[1,0,0]
	v_fma_mix_f32 v19, v46, v30, v19 op_sel:[1,0,0] op_sel_hi:[1,0,0]
	v_fma_mix_f32 v20, v47, v30, v20 op_sel_hi:[1,0,0]
	v_fma_mix_f32 v21, v47, v30, v21 op_sel:[1,0,0] op_sel_hi:[1,0,0]
	s_waitcnt vmcnt(0)
	v_cvt_scalef32_pk_f16_fp8 v44, v36, 1.0
	v_cvt_scalef32_pk_f16_fp8 v45, v36, 1.0 op_sel:[1,0,0]
	v_cvt_scalef32_pk_f16_fp8 v46, v37, 1.0
	v_cvt_scalef32_pk_f16_fp8 v47, v37, 1.0 op_sel:[1,0,0]
	v_fma_mix_f32 v14, v44, v31, v14 op_sel_hi:[1,0,0]
	v_fma_mix_f32 v15, v44, v31, v15 op_sel:[1,0,0] op_sel_hi:[1,0,0]
	v_fma_mix_f32 v16, v45, v31, v16 op_sel_hi:[1,0,0]
	v_fma_mix_f32 v17, v45, v31, v17 op_sel:[1,0,0] op_sel_hi:[1,0,0]
	v_fma_mix_f32 v18, v46, v31, v18 op_sel_hi:[1,0,0]
	v_fma_mix_f32 v19, v46, v31, v19 op_sel:[1,0,0] op_sel_hi:[1,0,0]
	v_fma_mix_f32 v20, v47, v31, v20 op_sel_hi:[1,0,0]
	v_fma_mix_f32 v21, v47, v31, v21 op_sel:[1,0,0] op_sel_hi:[1,0,0]
	s_branch .Lagg_epi
.Lagg_d1:
	s_cmp_lt_i32 s29, 9
	s_cbranch_scc1 .Lagg_epi
	s_cmp_lt_i32 s29, 11
	s_cbranch_scc1 .Lagg_s2h
	v_or_b32_dpp v22, v5, v1 row_newbcast:8 row_mask:0xf bank_mask:0xf
	v_or_b32_dpp v23, v5, v1 row_newbcast:9 row_mask:0xf bank_mask:0xf
	v_or_b32_dpp v24, v5, v1 row_newbcast:10 row_mask:0xf bank_mask:0xf
	v_or_b32_dpp v25, v5, v1 row_newbcast:11 row_mask:0xf bank_mask:0xf
	global_load_ushort v30, v22, s[6:7]
	global_load_ushort v31, v23, s[6:7]
	global_load_ushort v32, v24, s[6:7]
	global_load_ushort v33, v25, s[6:7]
	v_lshl_or_b32 v26, v22, 3, v2
	v_lshl_or_b32 v27, v23, 3, v2
	v_lshl_or_b32 v28, v24, 3, v2
	v_lshl_or_b32 v29, v25, 3, v2
	global_load_dwordx2 v[34:35], v26, s[4:5]
	global_load_dwordx2 v[36:37], v27, s[4:5]
	global_load_dwordx2 v[38:39], v28, s[4:5]
	global_load_dwordx2 v[40:41], v29, s[4:5]
	s_waitcnt vmcnt(4)
	v_fma_mix_f32 v30, v30, 1.0, v7 op_sel_hi:[1,0,0]
	v_fma_mix_f32 v31, v31, 1.0, v7 op_sel_hi:[1,0,0]
	v_fma_mix_f32 v32, v32, 1.0, v7 op_sel_hi:[1,0,0]
	v_fma_mix_f32 v33, v33, 1.0, v7 op_sel_hi:[1,0,0]
	v_mul_f32_e32 v44, 0x3e4ccccd, v30
	v_mul_f32_e32 v45, 0x3e4ccccd, v31
	v_mul_f32_e32 v46, 0x3e4ccccd, v32
	v_mul_f32_e32 v47, 0x3e4ccccd, v33
	v_max_f32_e32 v30, v30, v44
	v_max_f32_e32 v31, v31, v45
	v_max_f32_e32 v32, v32, v46
	v_max_f32_e32 v33, v33, v47
	v_max3_f32 v42, v11, v30, v31
	v_max3_f32 v12, v42, v32, v33
	v_sub_f32_e32 v43, v11, v12
	v_sub_f32_e32 v30, v30, v12
	v_sub_f32_e32 v31, v31, v12
	v_sub_f32_e32 v32, v32, v12
	v_sub_f32_e32 v33, v33, v12
	v_exp_f32_e32 v43, v43
	v_exp_f32_e32 v30, v30
	v_exp_f32_e32 v31, v31
	v_exp_f32_e32 v32, v32
	v_exp_f32_e32 v33, v33
	v_fma_f32 v13, v13, v43, v30
	v_mul_f32_e32 v14, v14, v43
	v_mul_f32_e32 v15, v15, v43
	v_mul_f32_e32 v16, v16, v43
	v_mul_f32_e32 v17, v17, v43
	v_mul_f32_e32 v18, v18, v43
	v_mul_f32_e32 v19, v19, v43
	v_mul_f32_e32 v20, v20, v43
	v_mul_f32_e32 v21, v21, v43
	v_add_f32_e32 v13, v13, v31
	v_add_f32_e32 v13, v13, v32
	v_add_f32_e32 v13, v13, v33
	s_waitcnt vmcnt(3)
	v_cvt_scalef32_pk_f16_fp8 v44, v34, 1.0
	v_cvt_scalef32_pk_f16_fp8 v45, v34, 1.0 op_sel:[1,0,0]
	v_cvt_scalef32_pk_f16_fp8 v46, v35, 1.0
	v_cvt_scalef32_pk_f16_fp8 v47, v35, 1.0 op_sel:[1,0,0]
	v_fma_mix_f32 v14, v44, v30, v14 op_sel_hi:[1,0,0]
	v_fma_mix_f32 v15, v44, v30, v15 op_sel:[1,0,0] op_sel_hi:[1,0,0]
	v_fma_mix_f32 v16, v45, v30, v16 op_sel_hi:[1,0,0]
	v_fma_mix_f32 v17, v45, v30, v17 op_sel:[1,0,0] op_sel_hi:[1,0,0]
	v_fma_mix_f32 v18, v46, v30, v18 op_sel_hi:[1,0,0]
	v_fma_mix_f32 v19, v46, v30, v19 op_sel:[1,0,0] op_sel_hi:[1,0,0]
	v_fma_mix_f32 v20, v47, v30, v20 op_sel_hi:[1,0,0]
	v_fma_mix_f32 v21, v47, v30, v21 op_sel:[1,0,0] op_sel_hi:[1,0,0]
	s_waitcnt vmcnt(2)
	v_cvt_scalef32_pk_f16_fp8 v44, v36, 1.0
	v_cvt_scalef32_pk_f16_fp8 v45, v36, 1.0 op_sel:[1,0,0]
	v_cvt_scalef32_pk_f16_fp8 v46, v37, 1.0
	v_cvt_scalef32_pk_f16_fp8 v47, v37, 1.0 op_sel:[1,0,0]
	v_fma_mix_f32 v14, v44, v31, v14 op_sel_hi:[1,0,0]
	v_fma_mix_f32 v15, v44, v31, v15 op_sel:[1,0,0] op_sel_hi:[1,0,0]
	v_fma_mix_f32 v16, v45, v31, v16 op_sel_hi:[1,0,0]
	v_fma_mix_f32 v17, v45, v31, v17 op_sel:[1,0,0] op_sel_hi:[1,0,0]
	v_fma_mix_f32 v18, v46, v31, v18 op_sel_hi:[1,0,0]
	v_fma_mix_f32 v19, v46, v31, v19 op_sel:[1,0,0] op_sel_hi:[1,0,0]
	v_fma_mix_f32 v20, v47, v31, v20 op_sel_hi:[1,0,0]
	v_fma_mix_f32 v21, v47, v31, v21 op_sel:[1,0,0] op_sel_hi:[1,0,0]
	s_waitcnt vmcnt(1)
	v_cvt_scalef32_pk_f16_fp8 v44, v38, 1.0
	v_cvt_scalef32_pk_f16_fp8 v45, v38, 1.0 op_sel:[1,0,0]
	v_cvt_scalef32_pk_f16_fp8 v46, v39, 1.0
	v_cvt_scalef32_pk_f16_fp8 v47, v39, 1.0 op_sel:[1,0,0]
	v_fma_mix_f32 v14, v44, v32, v14 op_sel_hi:[1,0,0]
	v_fma_mix_f32 v15, v44, v32, v15 op_sel:[1,0,0] op_sel_hi:[1,0,0]
	v_fma_mix_f32 v16, v45, v32, v16 op_sel_hi:[1,0,0]
	v_fma_mix_f32 v17, v45, v32, v17 op_sel:[1,0,0] op_sel_hi:[1,0,0]
	v_fma_mix_f32 v18, v46, v32, v18 op_sel_hi:[1,0,0]
	v_fma_mix_f32 v19, v46, v32, v19 op_sel:[1,0,0] op_sel_hi:[1,0,0]
	v_fma_mix_f32 v20, v47, v32, v20 op_sel_hi:[1,0,0]
	v_fma_mix_f32 v21, v47, v32, v21 op_sel:[1,0,0] op_sel_hi:[1,0,0]
	s_waitcnt vmcnt(0)
	v_cvt_scalef32_pk_f16_fp8 v44, v40, 1.0
	v_cvt_scalef32_pk_f16_fp8 v45, v40, 1.0 op_sel:[1,0,0]
	v_cvt_scalef32_pk_f16_fp8 v46, v41, 1.0
	v_cvt_scalef32_pk_f16_fp8 v47, v41, 1.0 op_sel:[1,0,0]
	v_fma_mix_f32 v14, v44, v33, v14 op_sel_hi:[1,0,0]
	v_fma_mix_f32 v15, v44, v33, v15 op_sel:[1,0,0] op_sel_hi:[1,0,0]
	v_fma_mix_f32 v16, v45, v33, v16 op_sel_hi:[1,0,0]
	v_fma_mix_f32 v17, v45, v33, v17 op_sel:[1,0,0] op_sel_hi:[1,0,0]
	v_fma_mix_f32 v18, v46, v33, v18 op_sel_hi:[1,0,0]
	v_fma_mix_f32 v19, v46, v33, v19 op_sel:[1,0,0] op_sel_hi:[1,0,0]
	v_fma_mix_f32 v20, v47, v33, v20 op_sel_hi:[1,0,0]
	v_fma_mix_f32 v21, v47, v33, v21 op_sel:[1,0,0] op_sel_hi:[1,0,0]
	s_branch .Lagg_d2
.Lagg_s2h:
	v_or_b32_dpp v22, v5, v1 row_newbcast:8 row_mask:0xf bank_mask:0xf
	v_or_b32_dpp v23, v5, v1 row_newbcast:9 row_mask:0xf bank_mask:0xf
	global_load_ushort v30, v22, s[6:7]
	global_load_ushort v31, v23, s[6:7]
	v_lshl_or_b32 v26, v22, 3, v2
	v_lshl_or_b32 v27, v23, 3, v2
	global_load_dwordx2 v[34:35], v26, s[4:5]
	global_load_dwordx2 v[36:37], v27, s[4:5]
	s_waitcnt vmcnt(2)
	v_fma_mix_f32 v30, v30, 1.0, v7 op_sel_hi:[1,0,0]
	v_fma_mix_f32 v31, v31, 1.0, v7 op_sel_hi:[1,0,0]
	v_mul_f32_e32 v44, 0x3e4ccccd, v30
	v_mul_f32_e32 v45, 0x3e4ccccd, v31
	v_max_f32_e32 v30, v30, v44
	v_max_f32_e32 v31, v31, v45
	v_max3_f32 v12, v11, v30, v31
	v_sub_f32_e32 v43, v11, v12
	v_sub_f32_e32 v30, v30, v12
	v_sub_f32_e32 v31, v31, v12
	v_exp_f32_e32 v43, v43
	v_exp_f32_e32 v30, v30
	v_exp_f32_e32 v31, v31
	v_fma_f32 v13, v13, v43, v30
	v_mul_f32_e32 v14, v14, v43
	v_mul_f32_e32 v15, v15, v43
	v_mul_f32_e32 v16, v16, v43
	v_mul_f32_e32 v17, v17, v43
	v_mul_f32_e32 v18, v18, v43
	v_mul_f32_e32 v19, v19, v43
	v_mul_f32_e32 v20, v20, v43
	v_mul_f32_e32 v21, v21, v43
	v_add_f32_e32 v13, v13, v31
	s_waitcnt vmcnt(1)
	v_cvt_scalef32_pk_f16_fp8 v44, v34, 1.0
	v_cvt_scalef32_pk_f16_fp8 v45, v34, 1.0 op_sel:[1,0,0]
	v_cvt_scalef32_pk_f16_fp8 v46, v35, 1.0
	v_cvt_scalef32_pk_f16_fp8 v47, v35, 1.0 op_sel:[1,0,0]
	v_fma_mix_f32 v14, v44, v30, v14 op_sel_hi:[1,0,0]
	v_fma_mix_f32 v15, v44, v30, v15 op_sel:[1,0,0] op_sel_hi:[1,0,0]
	v_fma_mix_f32 v16, v45, v30, v16 op_sel_hi:[1,0,0]
	v_fma_mix_f32 v17, v45, v30, v17 op_sel:[1,0,0] op_sel_hi:[1,0,0]
	v_fma_mix_f32 v18, v46, v30, v18 op_sel_hi:[1,0,0]
	v_fma_mix_f32 v19, v46, v30, v19 op_sel:[1,0,0] op_sel_hi:[1,0,0]
	v_fma_mix_f32 v20, v47, v30, v20 op_sel_hi:[1,0,0]
	v_fma_mix_f32 v21, v47, v30, v21 op_sel:[1,0,0] op_sel_hi:[1,0,0]
	s_waitcnt vmcnt(0)
	v_cvt_scalef32_pk_f16_fp8 v44, v36, 1.0
	v_cvt_scalef32_pk_f16_fp8 v45, v36, 1.0 op_sel:[1,0,0]
	v_cvt_scalef32_pk_f16_fp8 v46, v37, 1.0
	v_cvt_scalef32_pk_f16_fp8 v47, v37, 1.0 op_sel:[1,0,0]
	v_fma_mix_f32 v14, v44, v31, v14 op_sel_hi:[1,0,0]
	v_fma_mix_f32 v15, v44, v31, v15 op_sel:[1,0,0] op_sel_hi:[1,0,0]
	v_fma_mix_f32 v16, v45, v31, v16 op_sel_hi:[1,0,0]
	v_fma_mix_f32 v17, v45, v31, v17 op_sel:[1,0,0] op_sel_hi:[1,0,0]
	v_fma_mix_f32 v18, v46, v31, v18 op_sel_hi:[1,0,0]
	v_fma_mix_f32 v19, v46, v31, v19 op_sel:[1,0,0] op_sel_hi:[1,0,0]
	v_fma_mix_f32 v20, v47, v31, v20 op_sel_hi:[1,0,0]
	v_fma_mix_f32 v21, v47, v31, v21 op_sel:[1,0,0] op_sel_hi:[1,0,0]
	s_branch .Lagg_epi
.Lagg_d2:
	s_cmp_lt_i32 s29, 13
	s_cbranch_scc1 .Lagg_epi
	s_cmp_lt_i32 s29, 15
	s_cbranch_scc1 .Lagg_s3h
	v_or_b32_dpp v22, v5, v1 row_newbcast:12 row_mask:0xf bank_mask:0xf
	v_or_b32_dpp v23, v5, v1 row_newbcast:13 row_mask:0xf bank_mask:0xf
	v_or_b32_dpp v24, v5, v1 row_newbcast:14 row_mask:0xf bank_mask:0xf
	v_or_b32_dpp v25, v5, v1 row_newbcast:15 row_mask:0xf bank_mask:0xf
	global_load_ushort v30, v22, s[6:7]
	global_load_ushort v31, v23, s[6:7]
	global_load_ushort v32, v24, s[6:7]
	global_load_ushort v33, v25, s[6:7]
	v_lshl_or_b32 v26, v22, 3, v2
	v_lshl_or_b32 v27, v23, 3, v2
	v_lshl_or_b32 v28, v24, 3, v2
	v_lshl_or_b32 v29, v25, 3, v2
	global_load_dwordx2 v[34:35], v26, s[4:5]
	global_load_dwordx2 v[36:37], v27, s[4:5]
	global_load_dwordx2 v[38:39], v28, s[4:5]
	global_load_dwordx2 v[40:41], v29, s[4:5]
	s_waitcnt vmcnt(4)
	v_fma_mix_f32 v30, v30, 1.0, v7 op_sel_hi:[1,0,0]
	v_fma_mix_f32 v31, v31, 1.0, v7 op_sel_hi:[1,0,0]
	v_fma_mix_f32 v32, v32, 1.0, v7 op_sel_hi:[1,0,0]
	v_fma_mix_f32 v33, v33, 1.0, v7 op_sel_hi:[1,0,0]
	v_mul_f32_e32 v44, 0x3e4ccccd, v30
	v_mul_f32_e32 v45, 0x3e4ccccd, v31
	v_mul_f32_e32 v46, 0x3e4ccccd, v32
	v_mul_f32_e32 v47, 0x3e4ccccd, v33
	v_max_f32_e32 v30, v30, v44
	v_max_f32_e32 v31, v31, v45
	v_max_f32_e32 v32, v32, v46
	v_max_f32_e32 v33, v33, v47
	v_max3_f32 v42, v12, v30, v31
	v_max3_f32 v11, v42, v32, v33
	v_sub_f32_e32 v43, v12, v11
	v_sub_f32_e32 v30, v30, v11
	v_sub_f32_e32 v31, v31, v11
	v_sub_f32_e32 v32, v32, v11
	v_sub_f32_e32 v33, v33, v11
	v_exp_f32_e32 v43, v43
	v_exp_f32_e32 v30, v30
	v_exp_f32_e32 v31, v31
	v_exp_f32_e32 v32, v32
	v_exp_f32_e32 v33, v33
	v_fma_f32 v13, v13, v43, v30
	v_mul_f32_e32 v14, v14, v43
	v_mul_f32_e32 v15, v15, v43
	v_mul_f32_e32 v16, v16, v43
	v_mul_f32_e32 v17, v17, v43
	v_mul_f32_e32 v18, v18, v43
	v_mul_f32_e32 v19, v19, v43
	v_mul_f32_e32 v20, v20, v43
	v_mul_f32_e32 v21, v21, v43
	v_add_f32_e32 v13, v13, v31
	v_add_f32_e32 v13, v13, v32
	v_add_f32_e32 v13, v13, v33
	s_waitcnt vmcnt(3)
	v_cvt_scalef32_pk_f16_fp8 v44, v34, 1.0
	v_cvt_scalef32_pk_f16_fp8 v45, v34, 1.0 op_sel:[1,0,0]
	v_cvt_scalef32_pk_f16_fp8 v46, v35, 1.0
	v_cvt_scalef32_pk_f16_fp8 v47, v35, 1.0 op_sel:[1,0,0]
	v_fma_mix_f32 v14, v44, v30, v14 op_sel_hi:[1,0,0]
	v_fma_mix_f32 v15, v44, v30, v15 op_sel:[1,0,0] op_sel_hi:[1,0,0]
	v_fma_mix_f32 v16, v45, v30, v16 op_sel_hi:[1,0,0]
	v_fma_mix_f32 v17, v45, v30, v17 op_sel:[1,0,0] op_sel_hi:[1,0,0]
	v_fma_mix_f32 v18, v46, v30, v18 op_sel_hi:[1,0,0]
	v_fma_mix_f32 v19, v46, v30, v19 op_sel:[1,0,0] op_sel_hi:[1,0,0]
	v_fma_mix_f32 v20, v47, v30, v20 op_sel_hi:[1,0,0]
	v_fma_mix_f32 v21, v47, v30, v21 op_sel:[1,0,0] op_sel_hi:[1,0,0]
	s_waitcnt vmcnt(2)
	v_cvt_scalef32_pk_f16_fp8 v44, v36, 1.0
	v_cvt_scalef32_pk_f16_fp8 v45, v36, 1.0 op_sel:[1,0,0]
	v_cvt_scalef32_pk_f16_fp8 v46, v37, 1.0
	v_cvt_scalef32_pk_f16_fp8 v47, v37, 1.0 op_sel:[1,0,0]
	v_fma_mix_f32 v14, v44, v31, v14 op_sel_hi:[1,0,0]
	v_fma_mix_f32 v15, v44, v31, v15 op_sel:[1,0,0] op_sel_hi:[1,0,0]
	v_fma_mix_f32 v16, v45, v31, v16 op_sel_hi:[1,0,0]
	v_fma_mix_f32 v17, v45, v31, v17 op_sel:[1,0,0] op_sel_hi:[1,0,0]
	v_fma_mix_f32 v18, v46, v31, v18 op_sel_hi:[1,0,0]
	v_fma_mix_f32 v19, v46, v31, v19 op_sel:[1,0,0] op_sel_hi:[1,0,0]
	v_fma_mix_f32 v20, v47, v31, v20 op_sel_hi:[1,0,0]
	v_fma_mix_f32 v21, v47, v31, v21 op_sel:[1,0,0] op_sel_hi:[1,0,0]
	s_waitcnt vmcnt(1)
	v_cvt_scalef32_pk_f16_fp8 v44, v38, 1.0
	v_cvt_scalef32_pk_f16_fp8 v45, v38, 1.0 op_sel:[1,0,0]
	v_cvt_scalef32_pk_f16_fp8 v46, v39, 1.0
	v_cvt_scalef32_pk_f16_fp8 v47, v39, 1.0 op_sel:[1,0,0]
	v_fma_mix_f32 v14, v44, v32, v14 op_sel_hi:[1,0,0]
	v_fma_mix_f32 v15, v44, v32, v15 op_sel:[1,0,0] op_sel_hi:[1,0,0]
	v_fma_mix_f32 v16, v45, v32, v16 op_sel_hi:[1,0,0]
	v_fma_mix_f32 v17, v45, v32, v17 op_sel:[1,0,0] op_sel_hi:[1,0,0]
	v_fma_mix_f32 v18, v46, v32, v18 op_sel_hi:[1,0,0]
	v_fma_mix_f32 v19, v46, v32, v19 op_sel:[1,0,0] op_sel_hi:[1,0,0]
	v_fma_mix_f32 v20, v47, v32, v20 op_sel_hi:[1,0,0]
	v_fma_mix_f32 v21, v47, v32, v21 op_sel:[1,0,0] op_sel_hi:[1,0,0]
	s_waitcnt vmcnt(0)
	v_cvt_scalef32_pk_f16_fp8 v44, v40, 1.0
	v_cvt_scalef32_pk_f16_fp8 v45, v40, 1.0 op_sel:[1,0,0]
	v_cvt_scalef32_pk_f16_fp8 v46, v41, 1.0
	v_cvt_scalef32_pk_f16_fp8 v47, v41, 1.0 op_sel:[1,0,0]
	v_fma_mix_f32 v14, v44, v33, v14 op_sel_hi:[1,0,0]
	v_fma_mix_f32 v15, v44, v33, v15 op_sel:[1,0,0] op_sel_hi:[1,0,0]
	v_fma_mix_f32 v16, v45, v33, v16 op_sel_hi:[1,0,0]
	v_fma_mix_f32 v17, v45, v33, v17 op_sel:[1,0,0] op_sel_hi:[1,0,0]
	v_fma_mix_f32 v18, v46, v33, v18 op_sel_hi:[1,0,0]
	v_fma_mix_f32 v19, v46, v33, v19 op_sel:[1,0,0] op_sel_hi:[1,0,0]
	v_fma_mix_f32 v20, v47, v33, v20 op_sel_hi:[1,0,0]
	v_fma_mix_f32 v21, v47, v33, v21 op_sel:[1,0,0] op_sel_hi:[1,0,0]
	s_branch .Lagg_d3
.Lagg_s3h:
	v_or_b32_dpp v22, v5, v1 row_newbcast:12 row_mask:0xf bank_mask:0xf
	v_or_b32_dpp v23, v5, v1 row_newbcast:13 row_mask:0xf bank_mask:0xf
	global_load_ushort v30, v22, s[6:7]
	global_load_ushort v31, v23, s[6:7]
	v_lshl_or_b32 v26, v22, 3, v2
	v_lshl_or_b32 v27, v23, 3, v2
	global_load_dwordx2 v[34:35], v26, s[4:5]
	global_load_dwordx2 v[36:37], v27, s[4:5]
	s_waitcnt vmcnt(2)
	v_fma_mix_f32 v30, v30, 1.0, v7 op_sel_hi:[1,0,0]
	v_fma_mix_f32 v31, v31, 1.0, v7 op_sel_hi:[1,0,0]
	v_mul_f32_e32 v44, 0x3e4ccccd, v30
	v_mul_f32_e32 v45, 0x3e4ccccd, v31
	v_max_f32_e32 v30, v30, v44
	v_max_f32_e32 v31, v31, v45
	v_max3_f32 v11, v12, v30, v31
	v_sub_f32_e32 v43, v12, v11
	v_sub_f32_e32 v30, v30, v11
	v_sub_f32_e32 v31, v31, v11
	v_exp_f32_e32 v43, v43
	v_exp_f32_e32 v30, v30
	v_exp_f32_e32 v31, v31
	v_fma_f32 v13, v13, v43, v30
	v_mul_f32_e32 v14, v14, v43
	v_mul_f32_e32 v15, v15, v43
	v_mul_f32_e32 v16, v16, v43
	v_mul_f32_e32 v17, v17, v43
	v_mul_f32_e32 v18, v18, v43
	v_mul_f32_e32 v19, v19, v43
	v_mul_f32_e32 v20, v20, v43
	v_mul_f32_e32 v21, v21, v43
	v_add_f32_e32 v13, v13, v31
	s_waitcnt vmcnt(1)
	v_cvt_scalef32_pk_f16_fp8 v44, v34, 1.0
	v_cvt_scalef32_pk_f16_fp8 v45, v34, 1.0 op_sel:[1,0,0]
	v_cvt_scalef32_pk_f16_fp8 v46, v35, 1.0
	v_cvt_scalef32_pk_f16_fp8 v47, v35, 1.0 op_sel:[1,0,0]
	v_fma_mix_f32 v14, v44, v30, v14 op_sel_hi:[1,0,0]
	v_fma_mix_f32 v15, v44, v30, v15 op_sel:[1,0,0] op_sel_hi:[1,0,0]
	v_fma_mix_f32 v16, v45, v30, v16 op_sel_hi:[1,0,0]
	v_fma_mix_f32 v17, v45, v30, v17 op_sel:[1,0,0] op_sel_hi:[1,0,0]
	v_fma_mix_f32 v18, v46, v30, v18 op_sel_hi:[1,0,0]
	v_fma_mix_f32 v19, v46, v30, v19 op_sel:[1,0,0] op_sel_hi:[1,0,0]
	v_fma_mix_f32 v20, v47, v30, v20 op_sel_hi:[1,0,0]
	v_fma_mix_f32 v21, v47, v30, v21 op_sel:[1,0,0] op_sel_hi:[1,0,0]
	s_waitcnt vmcnt(0)
	v_cvt_scalef32_pk_f16_fp8 v44, v36, 1.0
	v_cvt_scalef32_pk_f16_fp8 v45, v36, 1.0 op_sel:[1,0,0]
	v_cvt_scalef32_pk_f16_fp8 v46, v37, 1.0
	v_cvt_scalef32_pk_f16_fp8 v47, v37, 1.0 op_sel:[1,0,0]
	v_fma_mix_f32 v14, v44, v31, v14 op_sel_hi:[1,0,0]
	v_fma_mix_f32 v15, v44, v31, v15 op_sel:[1,0,0] op_sel_hi:[1,0,0]
	v_fma_mix_f32 v16, v45, v31, v16 op_sel_hi:[1,0,0]
	v_fma_mix_f32 v17, v45, v31, v17 op_sel:[1,0,0] op_sel_hi:[1,0,0]
	v_fma_mix_f32 v18, v46, v31, v18 op_sel_hi:[1,0,0]
	v_fma_mix_f32 v19, v46, v31, v19 op_sel:[1,0,0] op_sel_hi:[1,0,0]
	v_fma_mix_f32 v20, v47, v31, v20 op_sel_hi:[1,0,0]
	v_fma_mix_f32 v21, v47, v31, v21 op_sel:[1,0,0] op_sel_hi:[1,0,0]
	s_branch .Lagg_epi
.Lagg_d3:
	s_cmp_lt_i32 s29, 17
	s_cbranch_scc1 .Lagg_epi
	s_cmp_lt_i32 s29, 19
	s_cbranch_scc1 .Lagg_s4h
	v_or_b32_dpp v22, v6, v1 row_newbcast:0 row_mask:0xf bank_mask:0xf
	v_or_b32_dpp v23, v6, v1 row_newbcast:1 row_mask:0xf bank_mask:0xf
	v_or_b32_dpp v24, v6, v1 row_newbcast:2 row_mask:0xf bank_mask:0xf
	v_or_b32_dpp v25, v6, v1 row_newbcast:3 row_mask:0xf bank_mask:0xf
	global_load_ushort v30, v22, s[6:7]
	global_load_ushort v31, v23, s[6:7]
	global_load_ushort v32, v24, s[6:7]
	global_load_ushort v33, v25, s[6:7]
	v_lshl_or_b32 v26, v22, 3, v2
	v_lshl_or_b32 v27, v23, 3, v2
	v_lshl_or_b32 v28, v24, 3, v2
	v_lshl_or_b32 v29, v25, 3, v2
	global_load_dwordx2 v[34:35], v26, s[4:5]
	global_load_dwordx2 v[36:37], v27, s[4:5]
	global_load_dwordx2 v[38:39], v28, s[4:5]
	global_load_dwordx2 v[40:41], v29, s[4:5]
	s_waitcnt vmcnt(4)
	v_fma_mix_f32 v30, v30, 1.0, v7 op_sel_hi:[1,0,0]
	v_fma_mix_f32 v31, v31, 1.0, v7 op_sel_hi:[1,0,0]
	v_fma_mix_f32 v32, v32, 1.0, v7 op_sel_hi:[1,0,0]
	v_fma_mix_f32 v33, v33, 1.0, v7 op_sel_hi:[1,0,0]
	v_mul_f32_e32 v44, 0x3e4ccccd, v30
	v_mul_f32_e32 v45, 0x3e4ccccd, v31
	v_mul_f32_e32 v46, 0x3e4ccccd, v32
	v_mul_f32_e32 v47, 0x3e4ccccd, v33
	v_max_f32_e32 v30, v30, v44
	v_max_f32_e32 v31, v31, v45
	v_max_f32_e32 v32, v32, v46
	v_max_f32_e32 v33, v33, v47
	v_max3_f32 v42, v11, v30, v31
	v_max3_f32 v12, v42, v32, v33
	v_sub_f32_e32 v43, v11, v12
	v_sub_f32_e32 v30, v30, v12
	v_sub_f32_e32 v31, v31, v12
	v_sub_f32_e32 v32, v32, v12
	v_sub_f32_e32 v33, v33, v12
	v_exp_f32_e32 v43, v43
	v_exp_f32_e32 v30, v30
	v_exp_f32_e32 v31, v31
	v_exp_f32_e32 v32, v32
	v_exp_f32_e32 v33, v33
	v_fma_f32 v13, v13, v43, v30
	v_mul_f32_e32 v14, v14, v43
	v_mul_f32_e32 v15, v15, v43
	v_mul_f32_e32 v16, v16, v43
	v_mul_f32_e32 v17, v17, v43
	v_mul_f32_e32 v18, v18, v43
	v_mul_f32_e32 v19, v19, v43
	v_mul_f32_e32 v20, v20, v43
	v_mul_f32_e32 v21, v21, v43
	v_add_f32_e32 v13, v13, v31
	v_add_f32_e32 v13, v13, v32
	v_add_f32_e32 v13, v13, v33
	s_waitcnt vmcnt(3)
	v_cvt_scalef32_pk_f16_fp8 v44, v34, 1.0
	v_cvt_scalef32_pk_f16_fp8 v45, v34, 1.0 op_sel:[1,0,0]
	v_cvt_scalef32_pk_f16_fp8 v46, v35, 1.0
	v_cvt_scalef32_pk_f16_fp8 v47, v35, 1.0 op_sel:[1,0,0]
	v_fma_mix_f32 v14, v44, v30, v14 op_sel_hi:[1,0,0]
	v_fma_mix_f32 v15, v44, v30, v15 op_sel:[1,0,0] op_sel_hi:[1,0,0]
	v_fma_mix_f32 v16, v45, v30, v16 op_sel_hi:[1,0,0]
	v_fma_mix_f32 v17, v45, v30, v17 op_sel:[1,0,0] op_sel_hi:[1,0,0]
	v_fma_mix_f32 v18, v46, v30, v18 op_sel_hi:[1,0,0]
	v_fma_mix_f32 v19, v46, v30, v19 op_sel:[1,0,0] op_sel_hi:[1,0,0]
	v_fma_mix_f32 v20, v47, v30, v20 op_sel_hi:[1,0,0]
	v_fma_mix_f32 v21, v47, v30, v21 op_sel:[1,0,0] op_sel_hi:[1,0,0]
	s_waitcnt vmcnt(2)
	v_cvt_scalef32_pk_f16_fp8 v44, v36, 1.0
	v_cvt_scalef32_pk_f16_fp8 v45, v36, 1.0 op_sel:[1,0,0]
	v_cvt_scalef32_pk_f16_fp8 v46, v37, 1.0
	v_cvt_scalef32_pk_f16_fp8 v47, v37, 1.0 op_sel:[1,0,0]
	v_fma_mix_f32 v14, v44, v31, v14 op_sel_hi:[1,0,0]
	v_fma_mix_f32 v15, v44, v31, v15 op_sel:[1,0,0] op_sel_hi:[1,0,0]
	v_fma_mix_f32 v16, v45, v31, v16 op_sel_hi:[1,0,0]
	v_fma_mix_f32 v17, v45, v31, v17 op_sel:[1,0,0] op_sel_hi:[1,0,0]
	v_fma_mix_f32 v18, v46, v31, v18 op_sel_hi:[1,0,0]
	v_fma_mix_f32 v19, v46, v31, v19 op_sel:[1,0,0] op_sel_hi:[1,0,0]
	v_fma_mix_f32 v20, v47, v31, v20 op_sel_hi:[1,0,0]
	v_fma_mix_f32 v21, v47, v31, v21 op_sel:[1,0,0] op_sel_hi:[1,0,0]
	s_waitcnt vmcnt(1)
	v_cvt_scalef32_pk_f16_fp8 v44, v38, 1.0
	v_cvt_scalef32_pk_f16_fp8 v45, v38, 1.0 op_sel:[1,0,0]
	v_cvt_scalef32_pk_f16_fp8 v46, v39, 1.0
	v_cvt_scalef32_pk_f16_fp8 v47, v39, 1.0 op_sel:[1,0,0]
	v_fma_mix_f32 v14, v44, v32, v14 op_sel_hi:[1,0,0]
	v_fma_mix_f32 v15, v44, v32, v15 op_sel:[1,0,0] op_sel_hi:[1,0,0]
	v_fma_mix_f32 v16, v45, v32, v16 op_sel_hi:[1,0,0]
	v_fma_mix_f32 v17, v45, v32, v17 op_sel:[1,0,0] op_sel_hi:[1,0,0]
	v_fma_mix_f32 v18, v46, v32, v18 op_sel_hi:[1,0,0]
	v_fma_mix_f32 v19, v46, v32, v19 op_sel:[1,0,0] op_sel_hi:[1,0,0]
	v_fma_mix_f32 v20, v47, v32, v20 op_sel_hi:[1,0,0]
	v_fma_mix_f32 v21, v47, v32, v21 op_sel:[1,0,0] op_sel_hi:[1,0,0]
	s_waitcnt vmcnt(0)
	v_cvt_scalef32_pk_f16_fp8 v44, v40, 1.0
	v_cvt_scalef32_pk_f16_fp8 v45, v40, 1.0 op_sel:[1,0,0]
	v_cvt_scalef32_pk_f16_fp8 v46, v41, 1.0
	v_cvt_scalef32_pk_f16_fp8 v47, v41, 1.0 op_sel:[1,0,0]
	v_fma_mix_f32 v14, v44, v33, v14 op_sel_hi:[1,0,0]
	v_fma_mix_f32 v15, v44, v33, v15 op_sel:[1,0,0] op_sel_hi:[1,0,0]
	v_fma_mix_f32 v16, v45, v33, v16 op_sel_hi:[1,0,0]
	v_fma_mix_f32 v17, v45, v33, v17 op_sel:[1,0,0] op_sel_hi:[1,0,0]
	v_fma_mix_f32 v18, v46, v33, v18 op_sel_hi:[1,0,0]
	v_fma_mix_f32 v19, v46, v33, v19 op_sel:[1,0,0] op_sel_hi:[1,0,0]
	v_fma_mix_f32 v20, v47, v33, v20 op_sel_hi:[1,0,0]
	v_fma_mix_f32 v21, v47, v33, v21 op_sel:[1,0,0] op_sel_hi:[1,0,0]
	s_branch .Lagg_d4
.Lagg_s4h:
	v_or_b32_dpp v22, v6, v1 row_newbcast:0 row_mask:0xf bank_mask:0xf
	v_or_b32_dpp v23, v6, v1 row_newbcast:1 row_mask:0xf bank_mask:0xf
	global_load_ushort v30, v22, s[6:7]
	global_load_ushort v31, v23, s[6:7]
	v_lshl_or_b32 v26, v22, 3, v2
	v_lshl_or_b32 v27, v23, 3, v2
	global_load_dwordx2 v[34:35], v26, s[4:5]
	global_load_dwordx2 v[36:37], v27, s[4:5]
	s_waitcnt vmcnt(2)
	v_fma_mix_f32 v30, v30, 1.0, v7 op_sel_hi:[1,0,0]
	v_fma_mix_f32 v31, v31, 1.0, v7 op_sel_hi:[1,0,0]
	v_mul_f32_e32 v44, 0x3e4ccccd, v30
	v_mul_f32_e32 v45, 0x3e4ccccd, v31
	v_max_f32_e32 v30, v30, v44
	v_max_f32_e32 v31, v31, v45
	v_max3_f32 v12, v11, v30, v31
	v_sub_f32_e32 v43, v11, v12
	v_sub_f32_e32 v30, v30, v12
	v_sub_f32_e32 v31, v31, v12
	v_exp_f32_e32 v43, v43
	v_exp_f32_e32 v30, v30
	v_exp_f32_e32 v31, v31
	v_fma_f32 v13, v13, v43, v30
	v_mul_f32_e32 v14, v14, v43
	v_mul_f32_e32 v15, v15, v43
	v_mul_f32_e32 v16, v16, v43
	v_mul_f32_e32 v17, v17, v43
	v_mul_f32_e32 v18, v18, v43
	v_mul_f32_e32 v19, v19, v43
	v_mul_f32_e32 v20, v20, v43
	v_mul_f32_e32 v21, v21, v43
	v_add_f32_e32 v13, v13, v31
	s_waitcnt vmcnt(1)
	v_cvt_scalef32_pk_f16_fp8 v44, v34, 1.0
	v_cvt_scalef32_pk_f16_fp8 v45, v34, 1.0 op_sel:[1,0,0]
	v_cvt_scalef32_pk_f16_fp8 v46, v35, 1.0
	v_cvt_scalef32_pk_f16_fp8 v47, v35, 1.0 op_sel:[1,0,0]
	v_fma_mix_f32 v14, v44, v30, v14 op_sel_hi:[1,0,0]
	v_fma_mix_f32 v15, v44, v30, v15 op_sel:[1,0,0] op_sel_hi:[1,0,0]
	v_fma_mix_f32 v16, v45, v30, v16 op_sel_hi:[1,0,0]
	v_fma_mix_f32 v17, v45, v30, v17 op_sel:[1,0,0] op_sel_hi:[1,0,0]
	v_fma_mix_f32 v18, v46, v30, v18 op_sel_hi:[1,0,0]
	v_fma_mix_f32 v19, v46, v30, v19 op_sel:[1,0,0] op_sel_hi:[1,0,0]
	v_fma_mix_f32 v20, v47, v30, v20 op_sel_hi:[1,0,0]
	v_fma_mix_f32 v21, v47, v30, v21 op_sel:[1,0,0] op_sel_hi:[1,0,0]
	s_waitcnt vmcnt(0)
	v_cvt_scalef32_pk_f16_fp8 v44, v36, 1.0
	v_cvt_scalef32_pk_f16_fp8 v45, v36, 1.0 op_sel:[1,0,0]
	v_cvt_scalef32_pk_f16_fp8 v46, v37, 1.0
	v_cvt_scalef32_pk_f16_fp8 v47, v37, 1.0 op_sel:[1,0,0]
	v_fma_mix_f32 v14, v44, v31, v14 op_sel_hi:[1,0,0]
	v_fma_mix_f32 v15, v44, v31, v15 op_sel:[1,0,0] op_sel_hi:[1,0,0]
	v_fma_mix_f32 v16, v45, v31, v16 op_sel_hi:[1,0,0]
	v_fma_mix_f32 v17, v45, v31, v17 op_sel:[1,0,0] op_sel_hi:[1,0,0]
	v_fma_mix_f32 v18, v46, v31, v18 op_sel_hi:[1,0,0]
	v_fma_mix_f32 v19, v46, v31, v19 op_sel:[1,0,0] op_sel_hi:[1,0,0]
	v_fma_mix_f32 v20, v47, v31, v20 op_sel_hi:[1,0,0]
	v_fma_mix_f32 v21, v47, v31, v21 op_sel:[1,0,0] op_sel_hi:[1,0,0]
	s_branch .Lagg_epi
.Lagg_d4:
	s_cmp_lt_i32 s29, 21
	s_cbranch_scc1 .Lagg_epi
	s_cmp_lt_i32 s29, 23
	s_cbranch_scc1 .Lagg_s5h
	v_or_b32_dpp v22, v6, v1 row_newbcast:4 row_mask:0xf bank_mask:0xf
	v_or_b32_dpp v23, v6, v1 row_newbcast:5 row_mask:0xf bank_mask:0xf
	v_or_b32_dpp v24, v6, v1 row_newbcast:6 row_mask:0xf bank_mask:0xf
	v_or_b32_dpp v25, v6, v1 row_newbcast:7 row_mask:0xf bank_mask:0xf
	global_load_ushort v30, v22, s[6:7]
	global_load_ushort v31, v23, s[6:7]
	global_load_ushort v32, v24, s[6:7]
	global_load_ushort v33, v25, s[6:7]
	v_lshl_or_b32 v26, v22, 3, v2
	v_lshl_or_b32 v27, v23, 3, v2
	v_lshl_or_b32 v28, v24, 3, v2
	v_lshl_or_b32 v29, v25, 3, v2
	global_load_dwordx2 v[34:35], v26, s[4:5]
	global_load_dwordx2 v[36:37], v27, s[4:5]
	global_load_dwordx2 v[38:39], v28, s[4:5]
	global_load_dwordx2 v[40:41], v29, s[4:5]
	s_waitcnt vmcnt(4)
	v_fma_mix_f32 v30, v30, 1.0, v7 op_sel_hi:[1,0,0]
	v_fma_mix_f32 v31, v31, 1.0, v7 op_sel_hi:[1,0,0]
	v_fma_mix_f32 v32, v32, 1.0, v7 op_sel_hi:[1,0,0]
	v_fma_mix_f32 v33, v33, 1.0, v7 op_sel_hi:[1,0,0]
	v_mul_f32_e32 v44, 0x3e4ccccd, v30
	v_mul_f32_e32 v45, 0x3e4ccccd, v31
	v_mul_f32_e32 v46, 0x3e4ccccd, v32
	v_mul_f32_e32 v47, 0x3e4ccccd, v33
	v_max_f32_e32 v30, v30, v44
	v_max_f32_e32 v31, v31, v45
	v_max_f32_e32 v32, v32, v46
	v_max_f32_e32 v33, v33, v47
	v_max3_f32 v42, v12, v30, v31
	v_max3_f32 v11, v42, v32, v33
	v_sub_f32_e32 v43, v12, v11
	v_sub_f32_e32 v30, v30, v11
	v_sub_f32_e32 v31, v31, v11
	v_sub_f32_e32 v32, v32, v11
	v_sub_f32_e32 v33, v33, v11
	v_exp_f32_e32 v43, v43
	v_exp_f32_e32 v30, v30
	v_exp_f32_e32 v31, v31
	v_exp_f32_e32 v32, v32
	v_exp_f32_e32 v33, v33
	v_fma_f32 v13, v13, v43, v30
	v_mul_f32_e32 v14, v14, v43
	v_mul_f32_e32 v15, v15, v43
	v_mul_f32_e32 v16, v16, v43
	v_mul_f32_e32 v17, v17, v43
	v_mul_f32_e32 v18, v18, v43
	v_mul_f32_e32 v19, v19, v43
	v_mul_f32_e32 v20, v20, v43
	v_mul_f32_e32 v21, v21, v43
	v_add_f32_e32 v13, v13, v31
	v_add_f32_e32 v13, v13, v32
	v_add_f32_e32 v13, v13, v33
	s_waitcnt vmcnt(3)
	v_cvt_scalef32_pk_f16_fp8 v44, v34, 1.0
	v_cvt_scalef32_pk_f16_fp8 v45, v34, 1.0 op_sel:[1,0,0]
	v_cvt_scalef32_pk_f16_fp8 v46, v35, 1.0
	v_cvt_scalef32_pk_f16_fp8 v47, v35, 1.0 op_sel:[1,0,0]
	v_fma_mix_f32 v14, v44, v30, v14 op_sel_hi:[1,0,0]
	v_fma_mix_f32 v15, v44, v30, v15 op_sel:[1,0,0] op_sel_hi:[1,0,0]
	v_fma_mix_f32 v16, v45, v30, v16 op_sel_hi:[1,0,0]
	v_fma_mix_f32 v17, v45, v30, v17 op_sel:[1,0,0] op_sel_hi:[1,0,0]
	v_fma_mix_f32 v18, v46, v30, v18 op_sel_hi:[1,0,0]
	v_fma_mix_f32 v19, v46, v30, v19 op_sel:[1,0,0] op_sel_hi:[1,0,0]
	v_fma_mix_f32 v20, v47, v30, v20 op_sel_hi:[1,0,0]
	v_fma_mix_f32 v21, v47, v30, v21 op_sel:[1,0,0] op_sel_hi:[1,0,0]
	s_waitcnt vmcnt(2)
	v_cvt_scalef32_pk_f16_fp8 v44, v36, 1.0
	v_cvt_scalef32_pk_f16_fp8 v45, v36, 1.0 op_sel:[1,0,0]
	v_cvt_scalef32_pk_f16_fp8 v46, v37, 1.0
	v_cvt_scalef32_pk_f16_fp8 v47, v37, 1.0 op_sel:[1,0,0]
	v_fma_mix_f32 v14, v44, v31, v14 op_sel_hi:[1,0,0]
	v_fma_mix_f32 v15, v44, v31, v15 op_sel:[1,0,0] op_sel_hi:[1,0,0]
	v_fma_mix_f32 v16, v45, v31, v16 op_sel_hi:[1,0,0]
	v_fma_mix_f32 v17, v45, v31, v17 op_sel:[1,0,0] op_sel_hi:[1,0,0]
	v_fma_mix_f32 v18, v46, v31, v18 op_sel_hi:[1,0,0]
	v_fma_mix_f32 v19, v46, v31, v19 op_sel:[1,0,0] op_sel_hi:[1,0,0]
	v_fma_mix_f32 v20, v47, v31, v20 op_sel_hi:[1,0,0]
	v_fma_mix_f32 v21, v47, v31, v21 op_sel:[1,0,0] op_sel_hi:[1,0,0]
	s_waitcnt vmcnt(1)
	v_cvt_scalef32_pk_f16_fp8 v44, v38, 1.0
	v_cvt_scalef32_pk_f16_fp8 v45, v38, 1.0 op_sel:[1,0,0]
	v_cvt_scalef32_pk_f16_fp8 v46, v39, 1.0
	v_cvt_scalef32_pk_f16_fp8 v47, v39, 1.0 op_sel:[1,0,0]
	v_fma_mix_f32 v14, v44, v32, v14 op_sel_hi:[1,0,0]
	v_fma_mix_f32 v15, v44, v32, v15 op_sel:[1,0,0] op_sel_hi:[1,0,0]
	v_fma_mix_f32 v16, v45, v32, v16 op_sel_hi:[1,0,0]
	v_fma_mix_f32 v17, v45, v32, v17 op_sel:[1,0,0] op_sel_hi:[1,0,0]
	v_fma_mix_f32 v18, v46, v32, v18 op_sel_hi:[1,0,0]
	v_fma_mix_f32 v19, v46, v32, v19 op_sel:[1,0,0] op_sel_hi:[1,0,0]
	v_fma_mix_f32 v20, v47, v32, v20 op_sel_hi:[1,0,0]
	v_fma_mix_f32 v21, v47, v32, v21 op_sel:[1,0,0] op_sel_hi:[1,0,0]
	s_waitcnt vmcnt(0)
	v_cvt_scalef32_pk_f16_fp8 v44, v40, 1.0
	v_cvt_scalef32_pk_f16_fp8 v45, v40, 1.0 op_sel:[1,0,0]
	v_cvt_scalef32_pk_f16_fp8 v46, v41, 1.0
	v_cvt_scalef32_pk_f16_fp8 v47, v41, 1.0 op_sel:[1,0,0]
	v_fma_mix_f32 v14, v44, v33, v14 op_sel_hi:[1,0,0]
	v_fma_mix_f32 v15, v44, v33, v15 op_sel:[1,0,0] op_sel_hi:[1,0,0]
	v_fma_mix_f32 v16, v45, v33, v16 op_sel_hi:[1,0,0]
	v_fma_mix_f32 v17, v45, v33, v17 op_sel:[1,0,0] op_sel_hi:[1,0,0]
	v_fma_mix_f32 v18, v46, v33, v18 op_sel_hi:[1,0,0]
	v_fma_mix_f32 v19, v46, v33, v19 op_sel:[1,0,0] op_sel_hi:[1,0,0]
	v_fma_mix_f32 v20, v47, v33, v20 op_sel_hi:[1,0,0]
	v_fma_mix_f32 v21, v47, v33, v21 op_sel:[1,0,0] op_sel_hi:[1,0,0]
	s_branch .Lagg_d5
.Lagg_s5h:
	v_or_b32_dpp v22, v6, v1 row_newbcast:4 row_mask:0xf bank_mask:0xf
	v_or_b32_dpp v23, v6, v1 row_newbcast:5 row_mask:0xf bank_mask:0xf
	global_load_ushort v30, v22, s[6:7]
	global_load_ushort v31, v23, s[6:7]
	v_lshl_or_b32 v26, v22, 3, v2
	v_lshl_or_b32 v27, v23, 3, v2
	global_load_dwordx2 v[34:35], v26, s[4:5]
	global_load_dwordx2 v[36:37], v27, s[4:5]
	s_waitcnt vmcnt(2)
	v_fma_mix_f32 v30, v30, 1.0, v7 op_sel_hi:[1,0,0]
	v_fma_mix_f32 v31, v31, 1.0, v7 op_sel_hi:[1,0,0]
	v_mul_f32_e32 v44, 0x3e4ccccd, v30
	v_mul_f32_e32 v45, 0x3e4ccccd, v31
	v_max_f32_e32 v30, v30, v44
	v_max_f32_e32 v31, v31, v45
	v_max3_f32 v11, v12, v30, v31
	v_sub_f32_e32 v43, v12, v11
	v_sub_f32_e32 v30, v30, v11
	v_sub_f32_e32 v31, v31, v11
	v_exp_f32_e32 v43, v43
	v_exp_f32_e32 v30, v30
	v_exp_f32_e32 v31, v31
	v_fma_f32 v13, v13, v43, v30
	v_mul_f32_e32 v14, v14, v43
	v_mul_f32_e32 v15, v15, v43
	v_mul_f32_e32 v16, v16, v43
	v_mul_f32_e32 v17, v17, v43
	v_mul_f32_e32 v18, v18, v43
	v_mul_f32_e32 v19, v19, v43
	v_mul_f32_e32 v20, v20, v43
	v_mul_f32_e32 v21, v21, v43
	v_add_f32_e32 v13, v13, v31
	s_waitcnt vmcnt(1)
	v_cvt_scalef32_pk_f16_fp8 v44, v34, 1.0
	v_cvt_scalef32_pk_f16_fp8 v45, v34, 1.0 op_sel:[1,0,0]
	v_cvt_scalef32_pk_f16_fp8 v46, v35, 1.0
	v_cvt_scalef32_pk_f16_fp8 v47, v35, 1.0 op_sel:[1,0,0]
	v_fma_mix_f32 v14, v44, v30, v14 op_sel_hi:[1,0,0]
	v_fma_mix_f32 v15, v44, v30, v15 op_sel:[1,0,0] op_sel_hi:[1,0,0]
	v_fma_mix_f32 v16, v45, v30, v16 op_sel_hi:[1,0,0]
	v_fma_mix_f32 v17, v45, v30, v17 op_sel:[1,0,0] op_sel_hi:[1,0,0]
	v_fma_mix_f32 v18, v46, v30, v18 op_sel_hi:[1,0,0]
	v_fma_mix_f32 v19, v46, v30, v19 op_sel:[1,0,0] op_sel_hi:[1,0,0]
	v_fma_mix_f32 v20, v47, v30, v20 op_sel_hi:[1,0,0]
	v_fma_mix_f32 v21, v47, v30, v21 op_sel:[1,0,0] op_sel_hi:[1,0,0]
	s_waitcnt vmcnt(0)
	v_cvt_scalef32_pk_f16_fp8 v44, v36, 1.0
	v_cvt_scalef32_pk_f16_fp8 v45, v36, 1.0 op_sel:[1,0,0]
	v_cvt_scalef32_pk_f16_fp8 v46, v37, 1.0
	v_cvt_scalef32_pk_f16_fp8 v47, v37, 1.0 op_sel:[1,0,0]
	v_fma_mix_f32 v14, v44, v31, v14 op_sel_hi:[1,0,0]
	v_fma_mix_f32 v15, v44, v31, v15 op_sel:[1,0,0] op_sel_hi:[1,0,0]
	v_fma_mix_f32 v16, v45, v31, v16 op_sel_hi:[1,0,0]
	v_fma_mix_f32 v17, v45, v31, v17 op_sel:[1,0,0] op_sel_hi:[1,0,0]
	v_fma_mix_f32 v18, v46, v31, v18 op_sel_hi:[1,0,0]
	v_fma_mix_f32 v19, v46, v31, v19 op_sel:[1,0,0] op_sel_hi:[1,0,0]
	v_fma_mix_f32 v20, v47, v31, v20 op_sel_hi:[1,0,0]
	v_fma_mix_f32 v21, v47, v31, v21 op_sel:[1,0,0] op_sel_hi:[1,0,0]
	s_branch .Lagg_epi
.Lagg_d5:
	s_cmp_lt_i32 s29, 25
	s_cbranch_scc1 .Lagg_epi
	s_cmp_lt_i32 s29, 27
	s_cbranch_scc1 .Lagg_s6h
	v_or_b32_dpp v22, v6, v1 row_newbcast:8 row_mask:0xf bank_mask:0xf
	v_or_b32_dpp v23, v6, v1 row_newbcast:9 row_mask:0xf bank_mask:0xf
	v_or_b32_dpp v24, v6, v1 row_newbcast:10 row_mask:0xf bank_mask:0xf
	v_or_b32_dpp v25, v6, v1 row_newbcast:11 row_mask:0xf bank_mask:0xf
	global_load_ushort v30, v22, s[6:7]
	global_load_ushort v31, v23, s[6:7]
	global_load_ushort v32, v24, s[6:7]
	global_load_ushort v33, v25, s[6:7]
	v_lshl_or_b32 v26, v22, 3, v2
	v_lshl_or_b32 v27, v23, 3, v2
	v_lshl_or_b32 v28, v24, 3, v2
	v_lshl_or_b32 v29, v25, 3, v2
	global_load_dwordx2 v[34:35], v26, s[4:5]
	global_load_dwordx2 v[36:37], v27, s[4:5]
	global_load_dwordx2 v[38:39], v28, s[4:5]
	global_load_dwordx2 v[40:41], v29, s[4:5]
	s_waitcnt vmcnt(4)
	v_fma_mix_f32 v30, v30, 1.0, v7 op_sel_hi:[1,0,0]
	v_fma_mix_f32 v31, v31, 1.0, v7 op_sel_hi:[1,0,0]
	v_fma_mix_f32 v32, v32, 1.0, v7 op_sel_hi:[1,0,0]
	v_fma_mix_f32 v33, v33, 1.0, v7 op_sel_hi:[1,0,0]
	v_mul_f32_e32 v44, 0x3e4ccccd, v30
	v_mul_f32_e32 v45, 0x3e4ccccd, v31
	v_mul_f32_e32 v46, 0x3e4ccccd, v32
	v_mul_f32_e32 v47, 0x3e4ccccd, v33
	v_max_f32_e32 v30, v30, v44
	v_max_f32_e32 v31, v31, v45
	v_max_f32_e32 v32, v32, v46
	v_max_f32_e32 v33, v33, v47
	v_max3_f32 v42, v11, v30, v31
	v_max3_f32 v12, v42, v32, v33
	v_sub_f32_e32 v43, v11, v12
	v_sub_f32_e32 v30, v30, v12
	v_sub_f32_e32 v31, v31, v12
	v_sub_f32_e32 v32, v32, v12
	v_sub_f32_e32 v33, v33, v12
	v_exp_f32_e32 v43, v43
	v_exp_f32_e32 v30, v30
	v_exp_f32_e32 v31, v31
	v_exp_f32_e32 v32, v32
	v_exp_f32_e32 v33, v33
	v_fma_f32 v13, v13, v43, v30
	v_mul_f32_e32 v14, v14, v43
	v_mul_f32_e32 v15, v15, v43
	v_mul_f32_e32 v16, v16, v43
	v_mul_f32_e32 v17, v17, v43
	v_mul_f32_e32 v18, v18, v43
	v_mul_f32_e32 v19, v19, v43
	v_mul_f32_e32 v20, v20, v43
	v_mul_f32_e32 v21, v21, v43
	v_add_f32_e32 v13, v13, v31
	v_add_f32_e32 v13, v13, v32
	v_add_f32_e32 v13, v13, v33
	s_waitcnt vmcnt(3)
	v_cvt_scalef32_pk_f16_fp8 v44, v34, 1.0
	v_cvt_scalef32_pk_f16_fp8 v45, v34, 1.0 op_sel:[1,0,0]
	v_cvt_scalef32_pk_f16_fp8 v46, v35, 1.0
	v_cvt_scalef32_pk_f16_fp8 v47, v35, 1.0 op_sel:[1,0,0]
	v_fma_mix_f32 v14, v44, v30, v14 op_sel_hi:[1,0,0]
	v_fma_mix_f32 v15, v44, v30, v15 op_sel:[1,0,0] op_sel_hi:[1,0,0]
	v_fma_mix_f32 v16, v45, v30, v16 op_sel_hi:[1,0,0]
	v_fma_mix_f32 v17, v45, v30, v17 op_sel:[1,0,0] op_sel_hi:[1,0,0]
	v_fma_mix_f32 v18, v46, v30, v18 op_sel_hi:[1,0,0]
	v_fma_mix_f32 v19, v46, v30, v19 op_sel:[1,0,0] op_sel_hi:[1,0,0]
	v_fma_mix_f32 v20, v47, v30, v20 op_sel_hi:[1,0,0]
	v_fma_mix_f32 v21, v47, v30, v21 op_sel:[1,0,0] op_sel_hi:[1,0,0]
	s_waitcnt vmcnt(2)
	v_cvt_scalef32_pk_f16_fp8 v44, v36, 1.0
	v_cvt_scalef32_pk_f16_fp8 v45, v36, 1.0 op_sel:[1,0,0]
	v_cvt_scalef32_pk_f16_fp8 v46, v37, 1.0
	v_cvt_scalef32_pk_f16_fp8 v47, v37, 1.0 op_sel:[1,0,0]
	v_fma_mix_f32 v14, v44, v31, v14 op_sel_hi:[1,0,0]
	v_fma_mix_f32 v15, v44, v31, v15 op_sel:[1,0,0] op_sel_hi:[1,0,0]
	v_fma_mix_f32 v16, v45, v31, v16 op_sel_hi:[1,0,0]
	v_fma_mix_f32 v17, v45, v31, v17 op_sel:[1,0,0] op_sel_hi:[1,0,0]
	v_fma_mix_f32 v18, v46, v31, v18 op_sel_hi:[1,0,0]
	v_fma_mix_f32 v19, v46, v31, v19 op_sel:[1,0,0] op_sel_hi:[1,0,0]
	v_fma_mix_f32 v20, v47, v31, v20 op_sel_hi:[1,0,0]
	v_fma_mix_f32 v21, v47, v31, v21 op_sel:[1,0,0] op_sel_hi:[1,0,0]
	s_waitcnt vmcnt(1)
	v_cvt_scalef32_pk_f16_fp8 v44, v38, 1.0
	v_cvt_scalef32_pk_f16_fp8 v45, v38, 1.0 op_sel:[1,0,0]
	v_cvt_scalef32_pk_f16_fp8 v46, v39, 1.0
	v_cvt_scalef32_pk_f16_fp8 v47, v39, 1.0 op_sel:[1,0,0]
	v_fma_mix_f32 v14, v44, v32, v14 op_sel_hi:[1,0,0]
	v_fma_mix_f32 v15, v44, v32, v15 op_sel:[1,0,0] op_sel_hi:[1,0,0]
	v_fma_mix_f32 v16, v45, v32, v16 op_sel_hi:[1,0,0]
	v_fma_mix_f32 v17, v45, v32, v17 op_sel:[1,0,0] op_sel_hi:[1,0,0]
	v_fma_mix_f32 v18, v46, v32, v18 op_sel_hi:[1,0,0]
	v_fma_mix_f32 v19, v46, v32, v19 op_sel:[1,0,0] op_sel_hi:[1,0,0]
	v_fma_mix_f32 v20, v47, v32, v20 op_sel_hi:[1,0,0]
	v_fma_mix_f32 v21, v47, v32, v21 op_sel:[1,0,0] op_sel_hi:[1,0,0]
	s_waitcnt vmcnt(0)
	v_cvt_scalef32_pk_f16_fp8 v44, v40, 1.0
	v_cvt_scalef32_pk_f16_fp8 v45, v40, 1.0 op_sel:[1,0,0]
	v_cvt_scalef32_pk_f16_fp8 v46, v41, 1.0
	v_cvt_scalef32_pk_f16_fp8 v47, v41, 1.0 op_sel:[1,0,0]
	v_fma_mix_f32 v14, v44, v33, v14 op_sel_hi:[1,0,0]
	v_fma_mix_f32 v15, v44, v33, v15 op_sel:[1,0,0] op_sel_hi:[1,0,0]
	v_fma_mix_f32 v16, v45, v33, v16 op_sel_hi:[1,0,0]
	v_fma_mix_f32 v17, v45, v33, v17 op_sel:[1,0,0] op_sel_hi:[1,0,0]
	v_fma_mix_f32 v18, v46, v33, v18 op_sel_hi:[1,0,0]
	v_fma_mix_f32 v19, v46, v33, v19 op_sel:[1,0,0] op_sel_hi:[1,0,0]
	v_fma_mix_f32 v20, v47, v33, v20 op_sel_hi:[1,0,0]
	v_fma_mix_f32 v21, v47, v33, v21 op_sel:[1,0,0] op_sel_hi:[1,0,0]
	s_branch .Lagg_d6
.Lagg_s6h:
	v_or_b32_dpp v22, v6, v1 row_newbcast:8 row_mask:0xf bank_mask:0xf
	v_or_b32_dpp v23, v6, v1 row_newbcast:9 row_mask:0xf bank_mask:0xf
	global_load_ushort v30, v22, s[6:7]
	global_load_ushort v31, v23, s[6:7]
	v_lshl_or_b32 v26, v22, 3, v2
	v_lshl_or_b32 v27, v23, 3, v2
	global_load_dwordx2 v[34:35], v26, s[4:5]
	global_load_dwordx2 v[36:37], v27, s[4:5]
	s_waitcnt vmcnt(2)
	v_fma_mix_f32 v30, v30, 1.0, v7 op_sel_hi:[1,0,0]
	v_fma_mix_f32 v31, v31, 1.0, v7 op_sel_hi:[1,0,0]
	v_mul_f32_e32 v44, 0x3e4ccccd, v30
	v_mul_f32_e32 v45, 0x3e4ccccd, v31
	v_max_f32_e32 v30, v30, v44
	v_max_f32_e32 v31, v31, v45
	v_max3_f32 v12, v11, v30, v31
	v_sub_f32_e32 v43, v11, v12
	v_sub_f32_e32 v30, v30, v12
	v_sub_f32_e32 v31, v31, v12
	v_exp_f32_e32 v43, v43
	v_exp_f32_e32 v30, v30
	v_exp_f32_e32 v31, v31
	v_fma_f32 v13, v13, v43, v30
	v_mul_f32_e32 v14, v14, v43
	v_mul_f32_e32 v15, v15, v43
	v_mul_f32_e32 v16, v16, v43
	v_mul_f32_e32 v17, v17, v43
	v_mul_f32_e32 v18, v18, v43
	v_mul_f32_e32 v19, v19, v43
	v_mul_f32_e32 v20, v20, v43
	v_mul_f32_e32 v21, v21, v43
	v_add_f32_e32 v13, v13, v31
	s_waitcnt vmcnt(1)
	v_cvt_scalef32_pk_f16_fp8 v44, v34, 1.0
	v_cvt_scalef32_pk_f16_fp8 v45, v34, 1.0 op_sel:[1,0,0]
	v_cvt_scalef32_pk_f16_fp8 v46, v35, 1.0
	v_cvt_scalef32_pk_f16_fp8 v47, v35, 1.0 op_sel:[1,0,0]
	v_fma_mix_f32 v14, v44, v30, v14 op_sel_hi:[1,0,0]
	v_fma_mix_f32 v15, v44, v30, v15 op_sel:[1,0,0] op_sel_hi:[1,0,0]
	v_fma_mix_f32 v16, v45, v30, v16 op_sel_hi:[1,0,0]
	v_fma_mix_f32 v17, v45, v30, v17 op_sel:[1,0,0] op_sel_hi:[1,0,0]
	v_fma_mix_f32 v18, v46, v30, v18 op_sel_hi:[1,0,0]
	v_fma_mix_f32 v19, v46, v30, v19 op_sel:[1,0,0] op_sel_hi:[1,0,0]
	v_fma_mix_f32 v20, v47, v30, v20 op_sel_hi:[1,0,0]
	v_fma_mix_f32 v21, v47, v30, v21 op_sel:[1,0,0] op_sel_hi:[1,0,0]
	s_waitcnt vmcnt(0)
	v_cvt_scalef32_pk_f16_fp8 v44, v36, 1.0
	v_cvt_scalef32_pk_f16_fp8 v45, v36, 1.0 op_sel:[1,0,0]
	v_cvt_scalef32_pk_f16_fp8 v46, v37, 1.0
	v_cvt_scalef32_pk_f16_fp8 v47, v37, 1.0 op_sel:[1,0,0]
	v_fma_mix_f32 v14, v44, v31, v14 op_sel_hi:[1,0,0]
	v_fma_mix_f32 v15, v44, v31, v15 op_sel:[1,0,0] op_sel_hi:[1,0,0]
	v_fma_mix_f32 v16, v45, v31, v16 op_sel_hi:[1,0,0]
	v_fma_mix_f32 v17, v45, v31, v17 op_sel:[1,0,0] op_sel_hi:[1,0,0]
	v_fma_mix_f32 v18, v46, v31, v18 op_sel_hi:[1,0,0]
	v_fma_mix_f32 v19, v46, v31, v19 op_sel:[1,0,0] op_sel_hi:[1,0,0]
	v_fma_mix_f32 v20, v47, v31, v20 op_sel_hi:[1,0,0]
	v_fma_mix_f32 v21, v47, v31, v21 op_sel:[1,0,0] op_sel_hi:[1,0,0]
	s_branch .Lagg_epi
.Lagg_d6:
	s_cmp_lt_i32 s29, 29
	s_cbranch_scc1 .Lagg_epi
	s_cmp_lt_i32 s29, 31
	s_cbranch_scc1 .Lagg_s7h
	v_or_b32_dpp v22, v6, v1 row_newbcast:12 row_mask:0xf bank_mask:0xf
	v_or_b32_dpp v23, v6, v1 row_newbcast:13 row_mask:0xf bank_mask:0xf
	v_or_b32_dpp v24, v6, v1 row_newbcast:14 row_mask:0xf bank_mask:0xf
	v_or_b32_dpp v25, v6, v1 row_newbcast:15 row_mask:0xf bank_mask:0xf
	global_load_ushort v30, v22, s[6:7]
	global_load_ushort v31, v23, s[6:7]
	global_load_ushort v32, v24, s[6:7]
	global_load_ushort v33, v25, s[6:7]
	v_lshl_or_b32 v26, v22, 3, v2
	v_lshl_or_b32 v27, v23, 3, v2
	v_lshl_or_b32 v28, v24, 3, v2
	v_lshl_or_b32 v29, v25, 3, v2
	global_load_dwordx2 v[34:35], v26, s[4:5]
	global_load_dwordx2 v[36:37], v27, s[4:5]
	global_load_dwordx2 v[38:39], v28, s[4:5]
	global_load_dwordx2 v[40:41], v29, s[4:5]
	s_waitcnt vmcnt(4)
	v_fma_mix_f32 v30, v30, 1.0, v7 op_sel_hi:[1,0,0]
	v_fma_mix_f32 v31, v31, 1.0, v7 op_sel_hi:[1,0,0]
	v_fma_mix_f32 v32, v32, 1.0, v7 op_sel_hi:[1,0,0]
	v_fma_mix_f32 v33, v33, 1.0, v7 op_sel_hi:[1,0,0]
	v_mul_f32_e32 v44, 0x3e4ccccd, v30
	v_mul_f32_e32 v45, 0x3e4ccccd, v31
	v_mul_f32_e32 v46, 0x3e4ccccd, v32
	v_mul_f32_e32 v47, 0x3e4ccccd, v33
	v_max_f32_e32 v30, v30, v44
	v_max_f32_e32 v31, v31, v45
	v_max_f32_e32 v32, v32, v46
	v_max_f32_e32 v33, v33, v47
	v_max3_f32 v42, v12, v30, v31
	v_max3_f32 v11, v42, v32, v33
	v_sub_f32_e32 v43, v12, v11
	v_sub_f32_e32 v30, v30, v11
	v_sub_f32_e32 v31, v31, v11
	v_sub_f32_e32 v32, v32, v11
	v_sub_f32_e32 v33, v33, v11
	v_exp_f32_e32 v43, v43
	v_exp_f32_e32 v30, v30
	v_exp_f32_e32 v31, v31
	v_exp_f32_e32 v32, v32
	v_exp_f32_e32 v33, v33
	v_fma_f32 v13, v13, v43, v30
	v_mul_f32_e32 v14, v14, v43
	v_mul_f32_e32 v15, v15, v43
	v_mul_f32_e32 v16, v16, v43
	v_mul_f32_e32 v17, v17, v43
	v_mul_f32_e32 v18, v18, v43
	v_mul_f32_e32 v19, v19, v43
	v_mul_f32_e32 v20, v20, v43
	v_mul_f32_e32 v21, v21, v43
	v_add_f32_e32 v13, v13, v31
	v_add_f32_e32 v13, v13, v32
	v_add_f32_e32 v13, v13, v33
	s_waitcnt vmcnt(3)
	v_cvt_scalef32_pk_f16_fp8 v44, v34, 1.0
	v_cvt_scalef32_pk_f16_fp8 v45, v34, 1.0 op_sel:[1,0,0]
	v_cvt_scalef32_pk_f16_fp8 v46, v35, 1.0
	v_cvt_scalef32_pk_f16_fp8 v47, v35, 1.0 op_sel:[1,0,0]
	v_fma_mix_f32 v14, v44, v30, v14 op_sel_hi:[1,0,0]
	v_fma_mix_f32 v15, v44, v30, v15 op_sel:[1,0,0] op_sel_hi:[1,0,0]
	v_fma_mix_f32 v16, v45, v30, v16 op_sel_hi:[1,0,0]
	v_fma_mix_f32 v17, v45, v30, v17 op_sel:[1,0,0] op_sel_hi:[1,0,0]
	v_fma_mix_f32 v18, v46, v30, v18 op_sel_hi:[1,0,0]
	v_fma_mix_f32 v19, v46, v30, v19 op_sel:[1,0,0] op_sel_hi:[1,0,0]
	v_fma_mix_f32 v20, v47, v30, v20 op_sel_hi:[1,0,0]
	v_fma_mix_f32 v21, v47, v30, v21 op_sel:[1,0,0] op_sel_hi:[1,0,0]
	s_waitcnt vmcnt(2)
	v_cvt_scalef32_pk_f16_fp8 v44, v36, 1.0
	v_cvt_scalef32_pk_f16_fp8 v45, v36, 1.0 op_sel:[1,0,0]
	v_cvt_scalef32_pk_f16_fp8 v46, v37, 1.0
	v_cvt_scalef32_pk_f16_fp8 v47, v37, 1.0 op_sel:[1,0,0]
	v_fma_mix_f32 v14, v44, v31, v14 op_sel_hi:[1,0,0]
	v_fma_mix_f32 v15, v44, v31, v15 op_sel:[1,0,0] op_sel_hi:[1,0,0]
	v_fma_mix_f32 v16, v45, v31, v16 op_sel_hi:[1,0,0]
	v_fma_mix_f32 v17, v45, v31, v17 op_sel:[1,0,0] op_sel_hi:[1,0,0]
	v_fma_mix_f32 v18, v46, v31, v18 op_sel_hi:[1,0,0]
	v_fma_mix_f32 v19, v46, v31, v19 op_sel:[1,0,0] op_sel_hi:[1,0,0]
	v_fma_mix_f32 v20, v47, v31, v20 op_sel_hi:[1,0,0]
	v_fma_mix_f32 v21, v47, v31, v21 op_sel:[1,0,0] op_sel_hi:[1,0,0]
	s_waitcnt vmcnt(1)
	v_cvt_scalef32_pk_f16_fp8 v44, v38, 1.0
	v_cvt_scalef32_pk_f16_fp8 v45, v38, 1.0 op_sel:[1,0,0]
	v_cvt_scalef32_pk_f16_fp8 v46, v39, 1.0
	v_cvt_scalef32_pk_f16_fp8 v47, v39, 1.0 op_sel:[1,0,0]
	v_fma_mix_f32 v14, v44, v32, v14 op_sel_hi:[1,0,0]
	v_fma_mix_f32 v15, v44, v32, v15 op_sel:[1,0,0] op_sel_hi:[1,0,0]
	v_fma_mix_f32 v16, v45, v32, v16 op_sel_hi:[1,0,0]
	v_fma_mix_f32 v17, v45, v32, v17 op_sel:[1,0,0] op_sel_hi:[1,0,0]
	v_fma_mix_f32 v18, v46, v32, v18 op_sel_hi:[1,0,0]
	v_fma_mix_f32 v19, v46, v32, v19 op_sel:[1,0,0] op_sel_hi:[1,0,0]
	v_fma_mix_f32 v20, v47, v32, v20 op_sel_hi:[1,0,0]
	v_fma_mix_f32 v21, v47, v32, v21 op_sel:[1,0,0] op_sel_hi:[1,0,0]
	s_waitcnt vmcnt(0)
	v_cvt_scalef32_pk_f16_fp8 v44, v40, 1.0
	v_cvt_scalef32_pk_f16_fp8 v45, v40, 1.0 op_sel:[1,0,0]
	v_cvt_scalef32_pk_f16_fp8 v46, v41, 1.0
	v_cvt_scalef32_pk_f16_fp8 v47, v41, 1.0 op_sel:[1,0,0]
	v_fma_mix_f32 v14, v44, v33, v14 op_sel_hi:[1,0,0]
	v_fma_mix_f32 v15, v44, v33, v15 op_sel:[1,0,0] op_sel_hi:[1,0,0]
	v_fma_mix_f32 v16, v45, v33, v16 op_sel_hi:[1,0,0]
	v_fma_mix_f32 v17, v45, v33, v17 op_sel:[1,0,0] op_sel_hi:[1,0,0]
	v_fma_mix_f32 v18, v46, v33, v18 op_sel_hi:[1,0,0]
	v_fma_mix_f32 v19, v46, v33, v19 op_sel:[1,0,0] op_sel_hi:[1,0,0]
	v_fma_mix_f32 v20, v47, v33, v20 op_sel_hi:[1,0,0]
	v_fma_mix_f32 v21, v47, v33, v21 op_sel:[1,0,0] op_sel_hi:[1,0,0]
	s_branch .Lagg_d7
.Lagg_s7h:
	v_or_b32_dpp v22, v6, v1 row_newbcast:12 row_mask:0xf bank_mask:0xf
	v_or_b32_dpp v23, v6, v1 row_newbcast:13 row_mask:0xf bank_mask:0xf
	global_load_ushort v30, v22, s[6:7]
	global_load_ushort v31, v23, s[6:7]
	v_lshl_or_b32 v26, v22, 3, v2
	v_lshl_or_b32 v27, v23, 3, v2
	global_load_dwordx2 v[34:35], v26, s[4:5]
	global_load_dwordx2 v[36:37], v27, s[4:5]
	s_waitcnt vmcnt(2)
	v_fma_mix_f32 v30, v30, 1.0, v7 op_sel_hi:[1,0,0]
	v_fma_mix_f32 v31, v31, 1.0, v7 op_sel_hi:[1,0,0]
	v_mul_f32_e32 v44, 0x3e4ccccd, v30
	v_mul_f32_e32 v45, 0x3e4ccccd, v31
	v_max_f32_e32 v30, v30, v44
	v_max_f32_e32 v31, v31, v45
	v_max3_f32 v11, v12, v30, v31
	v_sub_f32_e32 v43, v12, v11
	v_sub_f32_e32 v30, v30, v11
	v_sub_f32_e32 v31, v31, v11
	v_exp_f32_e32 v43, v43
	v_exp_f32_e32 v30, v30
	v_exp_f32_e32 v31, v31
	v_fma_f32 v13, v13, v43, v30
	v_mul_f32_e32 v14, v14, v43
	v_mul_f32_e32 v15, v15, v43
	v_mul_f32_e32 v16, v16, v43
	v_mul_f32_e32 v17, v17, v43
	v_mul_f32_e32 v18, v18, v43
	v_mul_f32_e32 v19, v19, v43
	v_mul_f32_e32 v20, v20, v43
	v_mul_f32_e32 v21, v21, v43
	v_add_f32_e32 v13, v13, v31
	s_waitcnt vmcnt(1)
	v_cvt_scalef32_pk_f16_fp8 v44, v34, 1.0
	v_cvt_scalef32_pk_f16_fp8 v45, v34, 1.0 op_sel:[1,0,0]
	v_cvt_scalef32_pk_f16_fp8 v46, v35, 1.0
	v_cvt_scalef32_pk_f16_fp8 v47, v35, 1.0 op_sel:[1,0,0]
	v_fma_mix_f32 v14, v44, v30, v14 op_sel_hi:[1,0,0]
	v_fma_mix_f32 v15, v44, v30, v15 op_sel:[1,0,0] op_sel_hi:[1,0,0]
	v_fma_mix_f32 v16, v45, v30, v16 op_sel_hi:[1,0,0]
	v_fma_mix_f32 v17, v45, v30, v17 op_sel:[1,0,0] op_sel_hi:[1,0,0]
	v_fma_mix_f32 v18, v46, v30, v18 op_sel_hi:[1,0,0]
	v_fma_mix_f32 v19, v46, v30, v19 op_sel:[1,0,0] op_sel_hi:[1,0,0]
	v_fma_mix_f32 v20, v47, v30, v20 op_sel_hi:[1,0,0]
	v_fma_mix_f32 v21, v47, v30, v21 op_sel:[1,0,0] op_sel_hi:[1,0,0]
	s_waitcnt vmcnt(0)
	v_cvt_scalef32_pk_f16_fp8 v44, v36, 1.0
	v_cvt_scalef32_pk_f16_fp8 v45, v36, 1.0 op_sel:[1,0,0]
	v_cvt_scalef32_pk_f16_fp8 v46, v37, 1.0
	v_cvt_scalef32_pk_f16_fp8 v47, v37, 1.0 op_sel:[1,0,0]
	v_fma_mix_f32 v14, v44, v31, v14 op_sel_hi:[1,0,0]
	v_fma_mix_f32 v15, v44, v31, v15 op_sel:[1,0,0] op_sel_hi:[1,0,0]
	v_fma_mix_f32 v16, v45, v31, v16 op_sel_hi:[1,0,0]
	v_fma_mix_f32 v17, v45, v31, v17 op_sel:[1,0,0] op_sel_hi:[1,0,0]
	v_fma_mix_f32 v18, v46, v31, v18 op_sel_hi:[1,0,0]
	v_fma_mix_f32 v19, v46, v31, v19 op_sel:[1,0,0] op_sel_hi:[1,0,0]
	v_fma_mix_f32 v20, v47, v31, v20 op_sel_hi:[1,0,0]
	v_fma_mix_f32 v21, v47, v31, v21 op_sel:[1,0,0] op_sel_hi:[1,0,0]
	s_branch .Lagg_epi
.Lagg_d7:
	s_cmp_lt_i32 s29, 33
	s_cbranch_scc1 .Lagg_epi
	s_sub_i32 s29, s29, 32
	s_add_i32 s42, s42, 32
	v_add_u32_e32 v31, s42, v53
	v_add_u32_e32 v30, v48, v31
	v_lshlrev_b32_e32 v30, 2, v30
	v_mov_b32_e32 v5, s24
	v_mov_b32_e32 v6, s24
	v_cmp_gt_i32_e32 vcc, v49, v31
	s_and_saveexec_b64 s[32:33], vcc
	global_load_dword v5, v30, s[12:13] offset:-4
	s_mov_b64 exec, s[32:33]
	v_add_u32_e32 v31, 16, v31
	v_cmp_gt_i32_e32 vcc, v49, v31
	s_and_saveexec_b64 s[32:33], vcc
	global_load_dword v6, v30, s[12:13] offset:60
	s_mov_b64 exec, s[32:33]
	s_waitcnt vmcnt(0)
	v_lshlrev_b32_e32 v5, 4, v5
	v_lshlrev_b32_e32 v6, 4, v6
	s_cmp_lt_i32 s29, 3
	s_cbranch_scc1 .Lagg_s0rh
	v_or_b32_dpp v22, v5, v1 row_newbcast:0 row_mask:0xf bank_mask:0xf
	v_or_b32_dpp v23, v5, v1 row_newbcast:1 row_mask:0xf bank_mask:0xf
	v_or_b32_dpp v24, v5, v1 row_newbcast:2 row_mask:0xf bank_mask:0xf
	v_or_b32_dpp v25, v5, v1 row_newbcast:3 row_mask:0xf bank_mask:0xf
	global_load_ushort v30, v22, s[6:7]
	global_load_ushort v31, v23, s[6:7]
	global_load_ushort v32, v24, s[6:7]
	global_load_ushort v33, v25, s[6:7]
	v_lshl_or_b32 v26, v22, 3, v2
	v_lshl_or_b32 v27, v23, 3, v2
	v_lshl_or_b32 v28, v24, 3, v2
	v_lshl_or_b32 v29, v25, 3, v2
	global_load_dwordx2 v[34:35], v26, s[4:5]
	global_load_dwordx2 v[36:37], v27, s[4:5]
	global_load_dwordx2 v[38:39], v28, s[4:5]
	global_load_dwordx2 v[40:41], v29, s[4:5]
	s_waitcnt vmcnt(4)
	v_fma_mix_f32 v30, v30, 1.0, v7 op_sel_hi:[1,0,0]
	v_fma_mix_f32 v31, v31, 1.0, v7 op_sel_hi:[1,0,0]
	v_fma_mix_f32 v32, v32, 1.0, v7 op_sel_hi:[1,0,0]
	v_fma_mix_f32 v33, v33, 1.0, v7 op_sel_hi:[1,0,0]
	v_mul_f32_e32 v44, 0x3e4ccccd, v30
	v_mul_f32_e32 v45, 0x3e4ccccd, v31
	v_mul_f32_e32 v46, 0x3e4ccccd, v32
	v_mul_f32_e32 v47, 0x3e4ccccd, v33
	v_max_f32_e32 v30, v30, v44
	v_max_f32_e32 v31, v31, v45
	v_max_f32_e32 v32, v32, v46
	v_max_f32_e32 v33, v33, v47
	v_max3_f32 v42, v11, v30, v31
	v_max3_f32 v12, v42, v32, v33
	v_sub_f32_e32 v43, v11, v12
	v_sub_f32_e32 v30, v30, v12
	v_sub_f32_e32 v31, v31, v12
	v_sub_f32_e32 v32, v32, v12
	v_sub_f32_e32 v33, v33, v12
	v_exp_f32_e32 v43, v43
	v_exp_f32_e32 v30, v30
	v_exp_f32_e32 v31, v31
	v_exp_f32_e32 v32, v32
	v_exp_f32_e32 v33, v33
	v_fma_f32 v13, v13, v43, v30
	v_mul_f32_e32 v14, v14, v43
	v_mul_f32_e32 v15, v15, v43
	v_mul_f32_e32 v16, v16, v43
	v_mul_f32_e32 v17, v17, v43
	v_mul_f32_e32 v18, v18, v43
	v_mul_f32_e32 v19, v19, v43
	v_mul_f32_e32 v20, v20, v43
	v_mul_f32_e32 v21, v21, v43
	v_add_f32_e32 v13, v13, v31
	v_add_f32_e32 v13, v13, v32
	v_add_f32_e32 v13, v13, v33
	s_waitcnt vmcnt(3)
	v_cvt_scalef32_pk_f16_fp8 v44, v34, 1.0
	v_cvt_scalef32_pk_f16_fp8 v45, v34, 1.0 op_sel:[1,0,0]
	v_cvt_scalef32_pk_f16_fp8 v46, v35, 1.0
	v_cvt_scalef32_pk_f16_fp8 v47, v35, 1.0 op_sel:[1,0,0]
	v_fma_mix_f32 v14, v44, v30, v14 op_sel_hi:[1,0,0]
	v_fma_mix_f32 v15, v44, v30, v15 op_sel:[1,0,0] op_sel_hi:[1,0,0]
	v_fma_mix_f32 v16, v45, v30, v16 op_sel_hi:[1,0,0]
	v_fma_mix_f32 v17, v45, v30, v17 op_sel:[1,0,0] op_sel_hi:[1,0,0]
	v_fma_mix_f32 v18, v46, v30, v18 op_sel_hi:[1,0,0]
	v_fma_mix_f32 v19, v46, v30, v19 op_sel:[1,0,0] op_sel_hi:[1,0,0]
	v_fma_mix_f32 v20, v47, v30, v20 op_sel_hi:[1,0,0]
	v_fma_mix_f32 v21, v47, v30, v21 op_sel:[1,0,0] op_sel_hi:[1,0,0]
	s_waitcnt vmcnt(2)
	v_cvt_scalef32_pk_f16_fp8 v44, v36, 1.0
	v_cvt_scalef32_pk_f16_fp8 v45, v36, 1.0 op_sel:[1,0,0]
	v_cvt_scalef32_pk_f16_fp8 v46, v37, 1.0
	v_cvt_scalef32_pk_f16_fp8 v47, v37, 1.0 op_sel:[1,0,0]
	v_fma_mix_f32 v14, v44, v31, v14 op_sel_hi:[1,0,0]
	v_fma_mix_f32 v15, v44, v31, v15 op_sel:[1,0,0] op_sel_hi:[1,0,0]
	v_fma_mix_f32 v16, v45, v31, v16 op_sel_hi:[1,0,0]
	v_fma_mix_f32 v17, v45, v31, v17 op_sel:[1,0,0] op_sel_hi:[1,0,0]
	v_fma_mix_f32 v18, v46, v31, v18 op_sel_hi:[1,0,0]
	v_fma_mix_f32 v19, v46, v31, v19 op_sel:[1,0,0] op_sel_hi:[1,0,0]
	v_fma_mix_f32 v20, v47, v31, v20 op_sel_hi:[1,0,0]
	v_fma_mix_f32 v21, v47, v31, v21 op_sel:[1,0,0] op_sel_hi:[1,0,0]
	s_waitcnt vmcnt(1)
	v_cvt_scalef32_pk_f16_fp8 v44, v38, 1.0
	v_cvt_scalef32_pk_f16_fp8 v45, v38, 1.0 op_sel:[1,0,0]
	v_cvt_scalef32_pk_f16_fp8 v46, v39, 1.0
	v_cvt_scalef32_pk_f16_fp8 v47, v39, 1.0 op_sel:[1,0,0]
	v_fma_mix_f32 v14, v44, v32, v14 op_sel_hi:[1,0,0]
	v_fma_mix_f32 v15, v44, v32, v15 op_sel:[1,0,0] op_sel_hi:[1,0,0]
	v_fma_mix_f32 v16, v45, v32, v16 op_sel_hi:[1,0,0]
	v_fma_mix_f32 v17, v45, v32, v17 op_sel:[1,0,0] op_sel_hi:[1,0,0]
	v_fma_mix_f32 v18, v46, v32, v18 op_sel_hi:[1,0,0]
	v_fma_mix_f32 v19, v46, v32, v19 op_sel:[1,0,0] op_sel_hi:[1,0,0]
	v_fma_mix_f32 v20, v47, v32, v20 op_sel_hi:[1,0,0]
	v_fma_mix_f32 v21, v47, v32, v21 op_sel:[1,0,0] op_sel_hi:[1,0,0]
	s_waitcnt vmcnt(0)
	v_cvt_scalef32_pk_f16_fp8 v44, v40, 1.0
	v_cvt_scalef32_pk_f16_fp8 v45, v40, 1.0 op_sel:[1,0,0]
	v_cvt_scalef32_pk_f16_fp8 v46, v41, 1.0
	v_cvt_scalef32_pk_f16_fp8 v47, v41, 1.0 op_sel:[1,0,0]
	v_fma_mix_f32 v14, v44, v33, v14 op_sel_hi:[1,0,0]
	v_fma_mix_f32 v15, v44, v33, v15 op_sel:[1,0,0] op_sel_hi:[1,0,0]
	v_fma_mix_f32 v16, v45, v33, v16 op_sel_hi:[1,0,0]
	v_fma_mix_f32 v17, v45, v33, v17 op_sel:[1,0,0] op_sel_hi:[1,0,0]
	v_fma_mix_f32 v18, v46, v33, v18 op_sel_hi:[1,0,0]
	v_fma_mix_f32 v19, v46, v33, v19 op_sel:[1,0,0] op_sel_hi:[1,0,0]
	v_fma_mix_f32 v20, v47, v33, v20 op_sel_hi:[1,0,0]
	v_fma_mix_f32 v21, v47, v33, v21 op_sel:[1,0,0] op_sel_hi:[1,0,0]
	s_branch .Lagg_c1
.Lagg_s0rh:
	v_or_b32_dpp v22, v5, v1 row_newbcast:0 row_mask:0xf bank_mask:0xf
	v_or_b32_dpp v23, v5, v1 row_newbcast:1 row_mask:0xf bank_mask:0xf
	global_load_ushort v30, v22, s[6:7]
	global_load_ushort v31, v23, s[6:7]
	v_lshl_or_b32 v26, v22, 3, v2
	v_lshl_or_b32 v27, v23, 3, v2
	global_load_dwordx2 v[34:35], v26, s[4:5]
	global_load_dwordx2 v[36:37], v27, s[4:5]
	s_waitcnt vmcnt(2)
	v_fma_mix_f32 v30, v30, 1.0, v7 op_sel_hi:[1,0,0]
	v_fma_mix_f32 v31, v31, 1.0, v7 op_sel_hi:[1,0,0]
	v_mul_f32_e32 v44, 0x3e4ccccd, v30
	v_mul_f32_e32 v45, 0x3e4ccccd, v31
	v_max_f32_e32 v30, v30, v44
	v_max_f32_e32 v31, v31, v45
	v_max3_f32 v12, v11, v30, v31
	v_sub_f32_e32 v43, v11, v12
	v_sub_f32_e32 v30, v30, v12
	v_sub_f32_e32 v31, v31, v12
	v_exp_f32_e32 v43, v43
	v_exp_f32_e32 v30, v30
	v_exp_f32_e32 v31, v31
	v_fma_f32 v13, v13, v43, v30
	v_mul_f32_e32 v14, v14, v43
	v_mul_f32_e32 v15, v15, v43
	v_mul_f32_e32 v16, v16, v43
	v_mul_f32_e32 v17, v17, v43
	v_mul_f32_e32 v18, v18, v43
	v_mul_f32_e32 v19, v19, v43
	v_mul_f32_e32 v20, v20, v43
	v_mul_f32_e32 v21, v21, v43
	v_add_f32_e32 v13, v13, v31
	s_waitcnt vmcnt(1)
	v_cvt_scalef32_pk_f16_fp8 v44, v34, 1.0
	v_cvt_scalef32_pk_f16_fp8 v45, v34, 1.0 op_sel:[1,0,0]
	v_cvt_scalef32_pk_f16_fp8 v46, v35, 1.0
	v_cvt_scalef32_pk_f16_fp8 v47, v35, 1.0 op_sel:[1,0,0]
	v_fma_mix_f32 v14, v44, v30, v14 op_sel_hi:[1,0,0]
	v_fma_mix_f32 v15, v44, v30, v15 op_sel:[1,0,0] op_sel_hi:[1,0,0]
	v_fma_mix_f32 v16, v45, v30, v16 op_sel_hi:[1,0,0]
	v_fma_mix_f32 v17, v45, v30, v17 op_sel:[1,0,0] op_sel_hi:[1,0,0]
	v_fma_mix_f32 v18, v46, v30, v18 op_sel_hi:[1,0,0]
	v_fma_mix_f32 v19, v46, v30, v19 op_sel:[1,0,0] op_sel_hi:[1,0,0]
	v_fma_mix_f32 v20, v47, v30, v20 op_sel_hi:[1,0,0]
	v_fma_mix_f32 v21, v47, v30, v21 op_sel:[1,0,0] op_sel_hi:[1,0,0]
	s_waitcnt vmcnt(0)
	v_cvt_scalef32_pk_f16_fp8 v44, v36, 1.0
	v_cvt_scalef32_pk_f16_fp8 v45, v36, 1.0 op_sel:[1,0,0]
	v_cvt_scalef32_pk_f16_fp8 v46, v37, 1.0
	v_cvt_scalef32_pk_f16_fp8 v47, v37, 1.0 op_sel:[1,0,0]
	v_fma_mix_f32 v14, v44, v31, v14 op_sel_hi:[1,0,0]
	v_fma_mix_f32 v15, v44, v31, v15 op_sel:[1,0,0] op_sel_hi:[1,0,0]
	v_fma_mix_f32 v16, v45, v31, v16 op_sel_hi:[1,0,0]
	v_fma_mix_f32 v17, v45, v31, v17 op_sel:[1,0,0] op_sel_hi:[1,0,0]
	v_fma_mix_f32 v18, v46, v31, v18 op_sel_hi:[1,0,0]
	v_fma_mix_f32 v19, v46, v31, v19 op_sel:[1,0,0] op_sel_hi:[1,0,0]
	v_fma_mix_f32 v20, v47, v31, v20 op_sel_hi:[1,0,0]
	v_fma_mix_f32 v21, v47, v31, v21 op_sel:[1,0,0] op_sel_hi:[1,0,0]
.Lagg_epi:
	s_and_saveexec_b64 s[32:33], s[36:37]
	ds_read_b128 v[22:25], v52
	ds_read_b128 v[26:29], v52 offset:512
	ds_read_b128 v[30:33], v52 offset:1024
	ds_read_b128 v[34:37], v52 offset:1536
	ds_read_b128 v[38:41], v52 offset:16
	ds_read_b128 v[42:45], v52 offset:528
	v_rcp_f32_e32 v46, v13
	s_waitcnt lgkmcnt(4)
	s_nop 0
	v_mul_f32_e32 v14, v14, v46
	v_mul_f32_e32 v15, v15, v46
	v_mul_f32_e32 v16, v16, v46
	v_mul_f32_e32 v17, v17, v46
	v_fma_f32 v14, v14, v22, v26
	v_fma_f32 v15, v15, v23, v27
	v_fma_f32 v16, v16, v24, v28
	v_fma_f32 v17, v17, v25, v29
	v_mul_f32_e32 v5, 0x3fb8aa3b, v14
	v_mul_f32_e32 v6, 0x3fb8aa3b, v15
	v_mul_f32_e32 v11, 0x3fb8aa3b, v16
	v_mul_f32_e32 v12, 0x3fb8aa3b, v17
	v_exp_f32_e32 v5, v5
	v_exp_f32_e32 v6, v6
	v_exp_f32_e32 v11, v11
	v_exp_f32_e32 v12, v12
	v_add_f32_e32 v5, -1.0, v5
	v_add_f32_e32 v6, -1.0, v6
	v_add_f32_e32 v11, -1.0, v11
	v_add_f32_e32 v12, -1.0, v12
	v_med3_f32 v14, v14, v5, 0
	v_med3_f32 v15, v15, v6, 0
	v_med3_f32 v16, v16, v11, 0
	v_med3_f32 v17, v17, v12, 0
	s_waitcnt lgkmcnt(2)
	v_mul_f32_e32 v47, v14, v30
	v_mul_f32_e32 v7, v14, v34
	v_fmac_f32_e32 v47, v15, v31
	v_fmac_f32_e32 v7, v15, v35
	v_fmac_f32_e32 v47, v16, v32
	v_fmac_f32_e32 v7, v16, v36
	v_fmac_f32_e32 v47, v17, v33
	v_fmac_f32_e32 v7, v17, v37
	v_cvt_f16_f32_e32 v5, v14
	v_cvt_f16_f32_e32 v6, v15
	v_cvt_f16_f32_e32 v11, v16
	v_cvt_f16_f32_e32 v12, v17
	ds_write_b16 v3, v5
	ds_write_b16 v3, v6 offset:16
	ds_write_b16 v3, v11 offset:32
	ds_write_b16 v3, v12 offset:48
	ds_read_b128 v[22:25], v52 offset:1040
	ds_read_b128 v[26:29], v52 offset:1552
	s_waitcnt lgkmcnt(6)
	v_mul_f32_e32 v18, v18, v46
	v_mul_f32_e32 v19, v19, v46
	v_mul_f32_e32 v20, v20, v46
	v_mul_f32_e32 v21, v21, v46
	v_fma_f32 v18, v18, v38, v42
	v_fma_f32 v19, v19, v39, v43
	v_fma_f32 v20, v20, v40, v44
	v_fma_f32 v21, v21, v41, v45
	v_mul_f32_e32 v5, 0x3fb8aa3b, v18
	v_mul_f32_e32 v6, 0x3fb8aa3b, v19
	v_mul_f32_e32 v11, 0x3fb8aa3b, v20
	v_mul_f32_e32 v12, 0x3fb8aa3b, v21
	v_exp_f32_e32 v5, v5
	v_exp_f32_e32 v6, v6
	v_exp_f32_e32 v11, v11
	v_exp_f32_e32 v12, v12
	v_add_f32_e32 v5, -1.0, v5
	v_add_f32_e32 v6, -1.0, v6
	v_add_f32_e32 v11, -1.0, v11
	v_add_f32_e32 v12, -1.0, v12
	v_med3_f32 v18, v18, v5, 0
	v_med3_f32 v19, v19, v6, 0
	v_med3_f32 v20, v20, v11, 0
	v_med3_f32 v21, v21, v12, 0
	s_waitcnt lgkmcnt(0)
	v_fmac_f32_e32 v47, v18, v22
	v_fmac_f32_e32 v7, v18, v26
	v_fmac_f32_e32 v47, v19, v23
	v_fmac_f32_e32 v7, v19, v27
	v_fmac_f32_e32 v47, v20, v24
	v_fmac_f32_e32 v7, v20, v28
	v_fmac_f32_e32 v47, v21, v25
	v_fmac_f32_e32 v7, v21, v29
	v_cvt_f16_f32_e32 v5, v18
	v_cvt_f16_f32_e32 v6, v19
	v_cvt_f16_f32_e32 v11, v20
	v_cvt_f16_f32_e32 v12, v21
	ds_write_b16 v3, v5 offset:64
	ds_write_b16 v3, v6 offset:80
	ds_write_b16 v3, v11 offset:96
	ds_write_b16 v3, v12 offset:112
	v_add_f32_dpp v47, v47, v47 row_ror:8 row_mask:0xf bank_mask:0xf
	v_add_f32_dpp v7, v7, v7 row_ror:8 row_mask:0xf bank_mask:0xf
	s_nop 0
	v_add_f32_dpp v47, v47, v47 row_ror:4 row_mask:0xf bank_mask:0xf
	v_add_f32_dpp v7, v7, v7 row_ror:4 row_mask:0xf bank_mask:0xf
	s_nop 0
	v_add_f32_dpp v47, v47, v47 row_ror:2 row_mask:0xf bank_mask:0xf
	v_add_f32_dpp v7, v7, v7 row_ror:2 row_mask:0xf bank_mask:0xf
	s_nop 0
	v_add_f32_dpp v47, v47, v47 row_ror:1 row_mask:0xf bank_mask:0xf
	v_add_f32_dpp v7, v7, v7 row_ror:1 row_mask:0xf bank_mask:0xf
	s_nop 0
	s_and_b64 exec, exec, s[34:35]
	global_store_dword v4, v47, s[20:21]
	global_store_dword v4, v7, s[22:23]
	s_mov_b64 exec, s[32:33]
	s_cmp_eq_u32 s31, 1
	s_cbranch_scc1 .Lagg_fin
	s_mov_b32 s31, 1
	v_mov_b32_e32 v5, v8
	v_mov_b32_e32 v6, v9
	v_mov_b32_e32 v7, v10
	v_mov_b32_e32 v48, v50
	v_mov_b32_e32 v49, v51
	s_mov_b32 s29, s30
	s_mov_b64 s[36:37], s[38:39]
	v_add_u32_e32 v4, 16, v4
	v_add_u32_e32 v3, 8, v3
	s_branch .Lagg_batch
.Lagg_fin:
	s_waitcnt lgkmcnt(0)
	ds_read_b128 v[22:25], v55
	ds_read_b128 v[26:29], v55 offset:16
	s_ashr_i32 s27, s26, 3
	s_lshl_b32 s27, s27, 11
	v_and_b32_e32 v30, 63, v0
	v_lshlrev_b32_e32 v30, 5, v30
	v_add_u32_e32 v30, s27, v30
	s_waitcnt lgkmcnt(0)
	global_store_dwordx4 v30, v[22:25], s[18:19]
	global_store_dwordx4 v30, v[26:29], s[18:19] offset:16

	.amdhsa_kernel _Z11agg1_kernelPKDF16_PKfS2_PKiS4_S2_S2_PDF16_PfS6_i
		.amdhsa_group_segment_fixed_size 10240
		.amdhsa_private_segment_fixed_size 0
		.amdhsa_kernarg_size 84
		.amdhsa_user_sgpr_count 2
		.amdhsa_user_sgpr_dispatch_ptr 0
		.amdhsa_user_sgpr_queue_ptr 0
		.amdhsa_user_sgpr_kernarg_segment_ptr 1
		.amdhsa_user_sgpr_dispatch_id 0
		.amdhsa_user_sgpr_kernarg_preload_length 0
		.amdhsa_user_sgpr_kernarg_preload_offset 0
		.amdhsa_user_sgpr_private_segment_size 0
		.amdhsa_uses_dynamic_stack 0
		.amdhsa_enable_private_segment 0
		.amdhsa_system_sgpr_workgroup_id_x 1
		.amdhsa_system_sgpr_workgroup_id_y 0
		.amdhsa_system_sgpr_workgroup_id_z 0
		.amdhsa_system_sgpr_workgroup_info 0
		.amdhsa_system_vgpr_workitem_id 0
		.amdhsa_next_free_vgpr 56
		.amdhsa_next_free_sgpr 44
		.amdhsa_accum_offset 56
		.amdhsa_reserve_vcc 1
		.amdhsa_float_round_mode_32 0
		.amdhsa_float_round_mode_16_64 0
		.amdhsa_float_denorm_mode_32 3
		.amdhsa_float_denorm_mode_16_64 3
		.amdhsa_dx10_clamp 1
		.amdhsa_ieee_mode 1
		.amdhsa_fp16_overflow 0
		.amdhsa_tg_split 0
		.amdhsa_exception_fp_ieee_invalid_op 0
		.amdhsa_exception_fp_denorm_src 0
		.amdhsa_exception_fp_ieee_div_zero 0
		.amdhsa_exception_fp_ieee_overflow 0
		.amdhsa_exception_fp_ieee_underflow 0
		.amdhsa_exception_fp_ieee_inexact 0
		.amdhsa_exception_int_div_zero 0
	.end_amdhsa_kernel

amdhsa.kernels:
  - .agpr_count:     0
    .args:
      - .actual_access:  read_only
        .address_space:  global
        .offset:         0
        .size:           8
        .value_kind:     global_buffer
      - .actual_access:  read_only
        .address_space:  global
        .offset:         8
        .size:           8
        .value_kind:     global_buffer
      - .actual_access:  read_only
        .address_space:  global
        .offset:         16
        .size:           8
        .value_kind:     global_buffer
      - .actual_access:  read_only
        .address_space:  global
        .offset:         24
        .size:           8
        .value_kind:     global_buffer
      - .actual_access:  read_only
        .address_space:  global
        .offset:         32
        .size:           8
        .value_kind:     global_buffer
      - .actual_access:  read_only
        .address_space:  global
        .offset:         40
        .size:           8
        .value_kind:     global_buffer
      - .actual_access:  read_only
        .address_space:  global
        .offset:         48
        .size:           8
        .value_kind:     global_buffer
      - .actual_access:  read_only
        .address_space:  global
        .offset:         56
        .size:           8
        .value_kind:     global_buffer
      - .actual_access:  read_only
        .address_space:  global
        .offset:         64
        .size:           8
        .value_kind:     global_buffer
      - .actual_access:  read_only
        .address_space:  global
        .offset:         72
        .size:           8
        .value_kind:     global_buffer
      - .actual_access:  read_only
        .address_space:  global
        .offset:         80
        .size:           8
        .value_kind:     global_buffer
      - .actual_access:  read_only
        .address_space:  global
        .offset:         88
        .size:           8
        .value_kind:     global_buffer
      - .actual_access:  read_only
        .address_space:  global
        .offset:         96
        .size:           8
        .value_kind:     global_buffer
      - .actual_access:  write_only
        .address_space:  global
        .offset:         104
        .size:           8
        .value_kind:     global_buffer
      - .actual_access:  write_only
        .address_space:  global
        .offset:         112
        .size:           8
        .value_kind:     global_buffer
      - .actual_access:  write_only
        .address_space:  global
        .offset:         120
        .size:           8
        .value_kind:     global_buffer
      - .actual_access:  write_only
        .address_space:  global
        .offset:         128
        .size:           8
        .value_kind:     global_buffer
      - .actual_access:  write_only
        .address_space:  global
        .offset:         136
        .size:           8
        .value_kind:     global_buffer
      - .actual_access:  write_only
        .address_space:  global
        .offset:         144
        .size:           8
        .value_kind:     global_buffer
      - .actual_access:  write_only
        .address_space:  global
        .offset:         152
        .size:           8
        .value_kind:     global_buffer
      - .actual_access:  write_only
        .address_space:  global
        .offset:         160
        .size:           8
        .value_kind:     global_buffer
      - .actual_access:  write_only
        .address_space:  global
        .offset:         168
        .size:           8
        .value_kind:     global_buffer
      - .actual_access:  read_only
        .address_space:  global
        .offset:         176
        .size:           8
        .value_kind:     global_buffer
    .group_segment_fixed_size: 29696
    .kernarg_segment_align: 8
    .kernarg_segment_size: 184
    .language:       OpenCL C
    .language_version:
      - 2
      - 0
    .max_flat_workgroup_size: 512
    .name:           _Z12front_kernelPKiS0_PKfS2_S2_S2_S2_S2_S2_S2_S2_S2_S2_PjS3_PiS4_PDF16_PfS6_S4_S5_S0_
    .private_segment_fixed_size: 0
    .sgpr_count:     30
    .sgpr_spill_count: 0
    .symbol:         _Z12front_kernelPKiS0_PKfS2_S2_S2_S2_S2_S2_S2_S2_S2_S2_PjS3_PiS4_PDF16_PfS6_S4_S5_S0_.kd
    .uniform_work_group_size: 1
    .uses_dynamic_stack: false
    .vgpr_count:     80
    .vgpr_spill_count: 0
    .wavefront_size: 64
  - .agpr_count:     0
    .args:
      - .actual_access:  read_only
        .address_space:  global
        .offset:         0
        .size:           8
        .value_kind:     global_buffer
      - .actual_access:  read_only
        .address_space:  global
        .offset:         8
        .size:           8
        .value_kind:     global_buffer
      - .actual_access:  write_only
        .address_space:  global
        .offset:         16
        .size:           8
        .value_kind:     global_buffer
      - .actual_access:  write_only
        .address_space:  global
        .offset:         24
        .size:           8
        .value_kind:     global_buffer
      - .actual_access:  write_only
        .address_space:  global
        .offset:         32
        .size:           8
        .value_kind:     global_buffer
      - .actual_access:  read_only
        .address_space:  global
        .offset:         40
        .size:           8
        .value_kind:     global_buffer
      - .actual_access:  read_only
        .address_space:  global
        .offset:         48
        .size:           8
        .value_kind:     global_buffer
      - .actual_access:  write_only
        .address_space:  global
        .offset:         56
        .size:           8
        .value_kind:     global_buffer
      - .actual_access:  write_only
        .address_space:  global
        .offset:         64
        .size:           8
        .value_kind:     global_buffer
    .group_segment_fixed_size: 40960
    .kernarg_segment_align: 8
    .kernarg_segment_size: 72
    .language:       OpenCL C
    .language_version:
      - 2
      - 0
    .max_flat_workgroup_size: 512
    .name:           _Z13second_kernelPKfPKDF16_PDF16_PfS4_PKjPKiPiS9_
    .private_segment_fixed_size: 0
    .sgpr_count:     29
    .sgpr_spill_count: 0
    .symbol:         _Z13second_kernelPKfPKDF16_PDF16_PfS4_PKjPKiPiS9_.kd
    .uniform_work_group_size: 1
    .uses_dynamic_stack: false
    .vgpr_count:     64
    .vgpr_spill_count: 0
    .wavefront_size: 64
  - .agpr_count:     0
    .args:
      - .actual_access:  read_only
        .address_space:  global
        .offset:         0
        .size:           8
        .value_kind:     global_buffer
      - .actual_access:  read_only
        .address_space:  global
        .offset:         8
        .size:           8
        .value_kind:     global_buffer
      - .actual_access:  read_only
        .address_space:  global
        .offset:         16
        .size:           8
        .value_kind:     global_buffer
      - .actual_access:  read_only
        .address_space:  global
        .offset:         24
        .size:           8
        .value_kind:     global_buffer
      - .actual_access:  read_only
        .address_space:  global
        .offset:         32
        .size:           8
        .value_kind:     global_buffer
      - .actual_access:  read_only
        .address_space:  global
        .offset:         40
        .size:           8
        .value_kind:     global_buffer
      - .actual_access:  read_only
        .address_space:  global
        .offset:         48
        .size:           8
        .value_kind:     global_buffer
      - .actual_access:  write_only
        .address_space:  global
        .offset:         56
        .size:           8
        .value_kind:     global_buffer
      - .actual_access:  write_only
        .address_space:  global
        .offset:         64
        .size:           8
        .value_kind:     global_buffer
      - .actual_access:  write_only
        .address_space:  global
        .offset:         72
        .size:           8
        .value_kind:     global_buffer
      - .offset:         80
        .size:           4
        .value_kind:     by_value
    .group_segment_fixed_size: 10240
    .kernarg_segment_align: 8
    .kernarg_segment_size: 84
    .language:       OpenCL C
    .language_version:
      - 2
      - 0
    .max_flat_workgroup_size: 256
    .name:           _Z11agg1_kernelPKDF16_PKfS2_PKiS4_S2_S2_PDF16_PfS6_i
    .private_segment_fixed_size: 0
    .sgpr_count:     50
    .sgpr_spill_count: 0
    .symbol:         _Z11agg1_kernelPKDF16_PKfS2_PKiS4_S2_S2_PDF16_PfS6_i.kd
    .uniform_work_group_size: 1
    .uses_dynamic_stack: false
    .vgpr_count:     56
    .vgpr_spill_count: 0
    .wavefront_size: 64
  - .agpr_count:     0
    .args:
      - .actual_access:  read_only
        .address_space:  global
        .offset:         0
        .size:           8
        .value_kind:     global_buffer
      - .actual_access:  read_only
        .address_space:  global
        .offset:         8
        .size:           8
        .value_kind:     global_buffer
      - .actual_access:  read_only
        .address_space:  global
        .offset:         16
        .size:           8
        .value_kind:     global_buffer
      - .actual_access:  read_only
        .address_space:  global
        .offset:         24
        .size:           8
        .value_kind:     global_buffer
      - .actual_access:  read_only
        .address_space:  global
        .offset:         32
        .size:           8
        .value_kind:     global_buffer
      - .actual_access:  write_only
        .address_space:  global
        .offset:         40
        .size:           8
        .value_kind:     global_buffer
      - .offset:         48
        .size:           4
        .value_kind:     by_value
    .group_segment_fixed_size: 0
    .kernarg_segment_align: 8
    .kernarg_segment_size: 52
    .language:       OpenCL C
    .language_version:
      - 2
      - 0
    .max_flat_workgroup_size: 256
    .name:           _Z13stats2_kernelPKiS0_PKfS2_S0_P15HIP_vector_typeIfLj4EEi
    .private_segment_fixed_size: 0
    .sgpr_count:     27
    .sgpr_spill_count: 0
    .symbol:         _Z13stats2_kernelPKiS0_PKfS2_S0_P15HIP_vector_typeIfLj4EEi.kd
    .uniform_work_group_size: 1
    .uses_dynamic_stack: false
    .vgpr_count:     32
    .vgpr_spill_count: 0
    .wavefront_size: 64
  - .agpr_count:     0
    .args:
      - .actual_access:  read_only
        .address_space:  global
        .offset:         0
        .size:           8
        .value_kind:     global_buffer
      - .actual_access:  read_only
        .address_space:  global
        .offset:         8
        .size:           8
        .value_kind:     global_buffer
      - .actual_access:  read_only
        .address_space:  global
        .offset:         16
        .size:           8
        .value_kind:     global_buffer
      - .actual_access:  read_only
        .address_space:  global
        .offset:         24
        .size:           8
        .value_kind:     global_buffer
      - .actual_access:  read_only
        .address_space:  global
        .offset:         32
        .size:           8
        .value_kind:     global_buffer
      - .actual_access:  write_only
        .address_space:  global
        .offset:         40
        .size:           8
        .value_kind:     global_buffer
      - .offset:         48
        .size:           4
        .value_kind:     by_value
    .group_segment_fixed_size: 69728
    .kernarg_segment_align: 8
    .kernarg_segment_size: 52
    .language:       OpenCL C
    .language_version:
      - 2
      - 0
    .max_flat_workgroup_size: 1024
    .name:           _Z12pool2_kernelPKjPKiPKfPK15HIP_vector_typeIfLj4EEPKDF16_Pfi
    .private_segment_fixed_size: 0
    .sgpr_count:     26
    .sgpr_spill_count: 0
    .symbol:         _Z12pool2_kernelPKjPKiPKfPK15HIP_vector_typeIfLj4EEPKDF16_Pfi.kd
    .uniform_work_group_size: 1
    .uses_dynamic_stack: false
    .vgpr_count:     123
    .vgpr_spill_count: 0
    .wavefront_size: 64
  - .agpr_count:     0
    .args:
      - .actual_access:  read_only
        .address_space:  global
        .offset:         0
        .size:           8
        .value_kind:     global_buffer
      - .actual_access:  read_only
        .address_space:  global
        .offset:         8
        .size:           8
        .value_kind:     global_buffer
      - .actual_access:  read_only
        .address_space:  global
        .offset:         16
        .size:           8
        .value_kind:     global_buffer
      - .actual_access:  read_only
        .address_space:  global
        .offset:         24
        .size:           8
        .value_kind:     global_buffer
      - .actual_access:  read_only
        .address_space:  global
        .offset:         32
        .size:           8
        .value_kind:     global_buffer
      - .actual_access:  read_only
        .address_space:  global
        .offset:         40
        .size:           8
        .value_kind:     global_buffer
      - .actual_access:  read_only
        .address_space:  global
        .offset:         48
        .size:           8
        .value_kind:     global_buffer
      - .actual_access:  read_only
        .address_space:  global
        .offset:         56
        .size:           8
        .value_kind:     global_buffer
      - .actual_access:  write_only
        .address_space:  global
        .offset:         64
        .size:           8
        .value_kind:     global_buffer
    .group_segment_fixed_size: 9472
    .kernarg_segment_align: 8
    .kernarg_segment_size: 72
    .language:       OpenCL C
    .language_version:
      - 2
      - 0
    .max_flat_workgroup_size: 1024
    .name:           _Z10mlp_kernelPKfPKiS0_S0_S0_S0_S0_S0_Pf
    .private_segment_fixed_size: 0
    .sgpr_count:     38
    .sgpr_spill_count: 0
    .symbol:         _Z10mlp_kernelPKfPKiS0_S0_S0_S0_S0_S0_Pf.kd
    .uniform_work_group_size: 1
    .uses_dynamic_stack: false
    .vgpr_count:     64
    .vgpr_spill_count: 0
    .wavefront_size: 64
